# v36 + first gate tiles of the merge epilogue requested inside the K-loop last iteration (after its last counted wait)
# speedup vs baseline: 1.0047x; 1.0016x over previous
;     __device__ __forceinline__ void a_ready(const Unit&) const { if (++ncall == 3 && sig != nullptr && threadIdx.x == 0) __hip_atomic_fetch_add(sig, 1u, __ATOMIC_RELAXED, __HIP_MEMORY_SCOPE_AGENT); }
; #define PG8_STAGE(bufoff, gbase, voff) do { _Pragma("unroll") for (int _i = 0; _i < 2; ++_i) \
;         __builtin_amdgcn_global_load_lds((const unsigned*)((const char*)(gbase) + (voff)[_i]), (PG8_LAS unsigned*)(lds + (bufoff) + ldsw + _i * 8192), 16, 0, 0); } while (0)
; #define PG8_LDA(dst, b, h) do { _Pragma("unroll") for (int m = 0; m < 4; ++m) _Pragma("unroll") for (int k = 0; k < 2; ++k) dst[m][k] = *(const PG8_LAS bf16x8*)(lds + PG8_SA(b, h) + aoff + m * 2048 + k * 1024); } while (0)
; #define PG8_LDB(dst, b, h) do { _Pragma("unroll") for (int n = 0; n < 2; ++n) _Pragma("unroll") for (int k = 0; k < 2; ++k) dst[n][k] = *(const PG8_LAS bf16x8*)(lds + PG8_SB(b, h) + boff + n * 2048 + k * 1024); } while (0)
; #define PG8_WAIT_V(n) asm volatile("s_waitcnt vmcnt(" #n ")" ::: "memory")
; #define PG8_WAIT_L(n) asm volatile("s_waitcnt lgkmcnt(" #n ")" ::: "memory")
; #define PG8_BAR __builtin_amdgcn_s_barrier()
; #define PG8_SCHED __builtin_amdgcn_sched_barrier(0)
; template <class Epi, class Sched, bool ALIGN_EPI = false, bool SP2 = false>
; __device__ __forceinline__ void gemm_phase(PG8_LAS unsigned char* lds, const Gemm g, const Sched& S, const Epi& E) {
;     ...
;         for (int t = 0; t < nt; t += 2) {
;             const bool last = (t == nt - 2);
;             const char* a1 = cA + (size_t)(t + 1) * kstep;
;             const char* a2 = last ? nA : cA + (size_t)(t + 2) * kstep; const char* b2 = last ? nB : cB + (size_t)(t + 2) * kstep;
;             const char* a3 = a2 + kstep; const char* b3 = b2 + kstep;
;             if (last && has_next) S.a_ready(nxt);
;             if constexpr (SP2) {
;             PG8_LDB(B0, 0, 0); PG8_LDB(B1, 0, 1); PG8_SCHED; PG8_LDA(At, 0, 0); PG8_STAGE(PG8_SA(1, 1), a1 + hstep, voffA);
;     ...
;             if (PROBE_KIND == 18 && t == 0 && ui > 0 && g.probe) { const unsigned long long tq_ = __builtin_amdgcn_s_memrealtime(); PG8_WAIT_V(8); pg8_probe_acc += (unsigned)(__builtin_amdgcn_s_memrealtime() - tq_); }
;     ...
;             PG8_WAIT_V(8); PG8_WAIT_L(0); PG8_BAR; PG8_MMA(0, 0, At, B0); PG8_MMA(0, 1, At, B1); PG8_BAR; PG8_SCHED;
.LBB0_1135:
	s_add_u32 s14, s6, 0xfffe0080
	s_addc_u32 s15, s7, -1
	s_add_i32 s65, 0, 0x10000
	s_cmp_eq_u32 s64, 4
	s_cselect_b32 s21, s1, s15
	s_cselect_b32 s20, s5, s14
	s_cselect_b32 s15, s19, s63
	s_cselect_b32 s14, s39, s62
	s_add_i32 s68, 0, 0x14000
	v_add_u32_e32 v72, s65, v201
	v_add_u32_e32 v136, s68, v201
	ds_read_b128 v[36:39], v72
	ds_read_b128 v[40:43], v72 offset:1024
	ds_read_b128 v[68:71], v72 offset:2048
	ds_read_b128 v[72:75], v72 offset:3072
	ds_read_b128 v[100:103], v136
	ds_read_b128 v[104:107], v136 offset:1024
	ds_read_b128 v[132:135], v136 offset:2048
	ds_read_b128 v[136:139], v136 offset:3072
	v_lshl_add_u64 v[198:199], s[6:7], 0, v[170:171]
	s_add_i32 m0, s28, 0xc000
	ds_read_b128 v[174:177], v203
	ds_read_b128 v[178:181], v203 offset:1024
	ds_read_b128 v[182:185], v203 offset:2048
	ds_read_b128 v[186:189], v203 offset:3072
	ds_read_b128 v[190:193], v203 offset:4096
	ds_read_b128 v[194:197], v203 offset:5120
	ds_read_b128 v[204:207], v203 offset:6144
	ds_read_b128 v[208:211], v203 offset:7168
	global_load_lds_dwordx4 v[198:199], off
	v_lshl_add_u64 v[198:199], s[6:7], 0, v[172:173]
	s_add_i32 m0, s28, 0xe000
	s_nop 0
	global_load_lds_dwordx4 v[198:199], off
	s_waitcnt vmcnt(8)
	s_waitcnt lgkmcnt(0)
	s_barrier
	s_setprio 1
	s_waitcnt lgkmcnt(0)
	v_mfma_f32_16x16x32_bf16 v[56:59], v[36:39], v[174:177], v[56:59]
	v_mfma_f32_16x16x32_bf16 v[52:55], v[68:71], v[174:177], v[52:55]
	v_mfma_f32_16x16x32_bf16 v[88:91], v[36:39], v[182:185], v[88:91]
	v_mfma_f32_16x16x32_bf16 v[84:87], v[68:71], v[182:185], v[84:87]
	v_mfma_f32_16x16x32_bf16 v[120:123], v[36:39], v[190:193], v[120:123]
	v_mfma_f32_16x16x32_bf16 v[116:119], v[68:71], v[190:193], v[116:119]
	v_mfma_f32_16x16x32_bf16 v[128:131], v[36:39], v[204:207], v[128:131]
	v_mfma_f32_16x16x32_bf16 v[124:127], v[68:71], v[204:207], v[124:127]
	v_mfma_f32_16x16x32_bf16 v[56:59], v[40:43], v[178:181], v[56:59]
	v_mfma_f32_16x16x32_bf16 v[52:55], v[72:75], v[178:181], v[52:55]
	v_mfma_f32_16x16x32_bf16 v[88:91], v[40:43], v[186:189], v[88:91]
	v_mfma_f32_16x16x32_bf16 v[84:87], v[72:75], v[186:189], v[84:87]
	v_mfma_f32_16x16x32_bf16 v[120:123], v[40:43], v[194:197], v[120:123]
	v_mfma_f32_16x16x32_bf16 v[116:119], v[72:75], v[194:197], v[116:119]
	v_mfma_f32_16x16x32_bf16 v[128:131], v[40:43], v[208:211], v[128:131]
	v_mfma_f32_16x16x32_bf16 v[124:127], v[72:75], v[208:211], v[124:127]
	s_setprio 0
	s_setprio 1
	v_mfma_f32_16x16x32_bf16 v[160:163], v[100:103], v[174:177], v[160:163]
	v_mfma_f32_16x16x32_bf16 v[156:159], v[132:135], v[174:177], v[156:159]
	v_mfma_f32_16x16x32_bf16 v[152:155], v[100:103], v[182:185], v[152:155]
	v_mfma_f32_16x16x32_bf16 v[148:151], v[132:135], v[182:185], v[148:151]
	v_mfma_f32_16x16x32_bf16 v[144:147], v[100:103], v[190:193], v[144:147]
	v_mfma_f32_16x16x32_bf16 v[140:143], v[132:135], v[190:193], v[140:143]
	v_mfma_f32_16x16x32_bf16 v[112:115], v[100:103], v[204:207], v[112:115]
	v_mfma_f32_16x16x32_bf16 v[108:111], v[132:135], v[204:207], v[108:111]
	v_mfma_f32_16x16x32_bf16 v[160:163], v[104:107], v[178:181], v[160:163]
	v_mfma_f32_16x16x32_bf16 v[156:159], v[136:139], v[178:181], v[156:159]
	v_mfma_f32_16x16x32_bf16 v[152:155], v[104:107], v[186:189], v[152:155]
	v_mfma_f32_16x16x32_bf16 v[148:151], v[136:139], v[186:189], v[148:151]
	v_mfma_f32_16x16x32_bf16 v[144:147], v[104:107], v[194:197], v[144:147]
	v_mfma_f32_16x16x32_bf16 v[140:143], v[136:139], v[194:197], v[140:143]
	v_mfma_f32_16x16x32_bf16 v[112:115], v[104:107], v[208:211], v[112:115]
	v_mfma_f32_16x16x32_bf16 v[108:111], v[136:139], v[208:211], v[108:111]
	s_setprio 0
	s_barrier
	s_add_i32 s65, s65, s27
	v_lshl_add_u64 v[198:199], s[14:15], 0, v[2:3]
	s_mov_b32 m0, s65
	ds_read_b128 v[174:177], v203 offset:16384
	ds_read_b128 v[178:181], v203 offset:17408
	ds_read_b128 v[182:185], v203 offset:18432
	ds_read_b128 v[186:189], v203 offset:19456
	ds_read_b128 v[190:193], v203 offset:20480
	ds_read_b128 v[194:197], v203 offset:21504
	ds_read_b128 v[204:207], v203 offset:22528
	ds_read_b128 v[208:211], v203 offset:23552
	global_load_lds_dwordx4 v[198:199], off
	s_add_i32 m0, s65, 0x2000
	s_add_u32 s66, s14, 0x20000
	v_lshl_add_u64 v[212:213], s[14:15], 0, v[168:169]
	s_addc_u32 s67, s15, 0
	s_add_i32 s65, s68, s27
	global_load_lds_dwordx4 v[212:213], off
	v_lshl_add_u64 v[214:215], s[66:67], 0, v[2:3]
	s_mov_b32 m0, s65
	v_lshl_add_u64 v[216:217], s[20:21], 0, v[166:167]
	global_load_lds_dwordx4 v[214:215], off
	v_lshl_add_u64 v[214:215], s[66:67], 0, v[168:169]
	s_add_i32 m0, s65, 0x2000
	s_nop 0
	global_load_lds_dwordx4 v[214:215], off
	v_lshl_add_u64 v[214:215], s[20:21], 0, v[164:165]
	s_mov_b32 m0, s28
	s_nop 0
	global_load_lds_dwordx4 v[214:215], off
	s_mov_b32 m0, s29
	s_nop 0
	global_load_lds_dwordx4 v[216:217], off
	s_waitcnt vmcnt(8)
	s_waitcnt lgkmcnt(0)
	s_barrier
; #define PG8_STAGE(bufoff, gbase, voff) do { _Pragma("unroll") for (int _i = 0; _i < 2; ++_i) \
;         __builtin_amdgcn_global_load_lds((const unsigned*)((const char*)(gbase) + (voff)[_i]), (PG8_LAS unsigned*)(lds + (bufoff) + ldsw + _i * 8192), 16, 0, 0); } while (0)
; #define PG8_LDA(dst, b, h) do { _Pragma("unroll") for (int m = 0; m < 4; ++m) _Pragma("unroll") for (int k = 0; k < 2; ++k) dst[m][k] = *(const PG8_LAS bf16x8*)(lds + PG8_SA(b, h) + aoff + m * 2048 + k * 1024); } while (0)
; #define PG8_LDB(dst, b, h) do { _Pragma("unroll") for (int n = 0; n < 2; ++n) _Pragma("unroll") for (int k = 0; k < 2; ++k) dst[n][k] = *(const PG8_LAS bf16x8*)(lds + PG8_SB(b, h) + boff + n * 2048 + k * 1024); } while (0)
; #define PG8_MMA(ai, bj, At, Bt) do { __builtin_amdgcn_s_setprio(1); _Pragma("unroll") for (int m = 0; m < 4; ++m) _Pragma("unroll") for (int n = 0; n < 2; ++n) _Pragma("unroll") for (int k = 0; k < 2; ++k) \
;         acc[ai][bj][m][n] = __builtin_amdgcn_mfma_f32_16x16x32_bf16(Bt[n][k], At[m][k], acc[ai][bj][m][n], 0, 0, 0); __builtin_amdgcn_s_setprio(0); } while (0)
; #define PG8_WAIT_V(n) asm volatile("s_waitcnt vmcnt(" #n ")" ::: "memory")
; #define PG8_WAIT_L(n) asm volatile("s_waitcnt lgkmcnt(" #n ")" ::: "memory")
; #define PG8_BAR __builtin_amdgcn_s_barrier()
; #define PG8_SCHED __builtin_amdgcn_sched_barrier(0)
; template <class Epi, class Sched, bool ALIGN_EPI = false, bool SP2 = false>
; __device__ __forceinline__ void gemm_phase(PG8_LAS unsigned char* lds, const Gemm g, const Sched& S, const Epi& E) {
;     ...
;             PG8_WAIT_V(8); PG8_WAIT_L(0); PG8_BAR; if (cur.half == 0) { PG8_MMA(1, 0, At, B0); PG8_MMA(1, 1, At, B1); } PG8_BAR; PG8_SCHED;
;             PG8_LDB(B0, 1, 0); PG8_LDB(B1, 1, 1); PG8_SCHED; PG8_LDA(At, 1, 0); PG8_STAGE(PG8_SA(0, 1), a2 + hstep, voffA);
;             PG8_WAIT_V(8); PG8_WAIT_L(0); PG8_BAR; PG8_MMA(0, 0, At, B0); PG8_MMA(0, 1, At, B1); PG8_BAR; PG8_SCHED;
	s_setprio 1
	s_waitcnt lgkmcnt(0)
	v_mfma_f32_16x16x32_bf16 v[96:99], v[36:39], v[174:177], v[96:99]
	v_mfma_f32_16x16x32_bf16 v[92:95], v[68:71], v[174:177], v[92:95]
	v_mfma_f32_16x16x32_bf16 v[64:67], v[36:39], v[182:185], v[64:67]
	v_mfma_f32_16x16x32_bf16 v[60:63], v[68:71], v[182:185], v[60:63]
	v_mfma_f32_16x16x32_bf16 v[32:35], v[36:39], v[190:193], v[32:35]
	v_mfma_f32_16x16x32_bf16 v[28:31], v[68:71], v[190:193], v[28:31]
	v_mfma_f32_16x16x32_bf16 v[16:19], v[36:39], v[204:207], v[16:19]
	v_mfma_f32_16x16x32_bf16 v[12:15], v[68:71], v[204:207], v[12:15]
	v_mfma_f32_16x16x32_bf16 v[96:99], v[40:43], v[178:181], v[96:99]
	v_mfma_f32_16x16x32_bf16 v[92:95], v[72:75], v[178:181], v[92:95]
	v_mfma_f32_16x16x32_bf16 v[64:67], v[40:43], v[186:189], v[64:67]
	v_mfma_f32_16x16x32_bf16 v[60:63], v[72:75], v[186:189], v[60:63]
	v_mfma_f32_16x16x32_bf16 v[32:35], v[40:43], v[194:197], v[32:35]
	v_mfma_f32_16x16x32_bf16 v[28:31], v[72:75], v[194:197], v[28:31]
	v_mfma_f32_16x16x32_bf16 v[16:19], v[40:43], v[208:211], v[16:19]
	v_mfma_f32_16x16x32_bf16 v[12:15], v[72:75], v[208:211], v[12:15]
	s_setprio 0
	s_setprio 1
	v_mfma_f32_16x16x32_bf16 v[48:51], v[100:103], v[182:185], v[48:51]
	v_mfma_f32_16x16x32_bf16 v[44:47], v[132:135], v[182:185], v[44:47]
	v_mfma_f32_16x16x32_bf16 v[24:27], v[100:103], v[190:193], v[24:27]
	v_mfma_f32_16x16x32_bf16 v[20:23], v[132:135], v[190:193], v[20:23]
	v_mfma_f32_16x16x32_bf16 v[8:11], v[100:103], v[204:207], v[8:11]
	v_mfma_f32_16x16x32_bf16 v[4:7], v[132:135], v[204:207], v[4:7]
	v_mfma_f32_16x16x32_bf16 v[36:39], v[100:103], v[174:177], v[80:83]
	v_mfma_f32_16x16x32_bf16 v[40:43], v[132:135], v[174:177], v[76:79]
	v_mfma_f32_16x16x32_bf16 v[48:51], v[104:107], v[186:189], v[48:51]
	v_mfma_f32_16x16x32_bf16 v[44:47], v[136:139], v[186:189], v[44:47]
	v_mfma_f32_16x16x32_bf16 v[24:27], v[104:107], v[194:197], v[24:27]
	v_mfma_f32_16x16x32_bf16 v[20:23], v[136:139], v[194:197], v[20:23]
	v_mfma_f32_16x16x32_bf16 v[8:11], v[104:107], v[208:211], v[8:11]
	v_mfma_f32_16x16x32_bf16 v[4:7], v[136:139], v[208:211], v[4:7]
	v_mfma_f32_16x16x32_bf16 v[36:39], v[104:107], v[178:181], v[36:39]
	v_mfma_f32_16x16x32_bf16 v[40:43], v[136:139], v[178:181], v[40:43]
	s_setprio 0
	s_barrier
	s_add_i32 s65, 0, 0x18000
	s_add_i32 s66, 0, 0x1c000
	v_add_u32_e32 v80, s65, v201
	v_add_u32_e32 v136, s66, v201
	ds_read_b128 v[68:71], v80
	ds_read_b128 v[72:75], v80 offset:1024
	ds_read_b128 v[76:79], v80 offset:2048
	ds_read_b128 v[80:83], v80 offset:3072
	ds_read_b128 v[100:103], v136
	ds_read_b128 v[104:107], v136 offset:1024
	ds_read_b128 v[132:135], v136 offset:2048
	ds_read_b128 v[136:139], v136 offset:3072
	s_add_u32 s20, s20, 0x20000
	s_addc_u32 s21, s21, 0
	s_mov_b32 m0, s30
	v_lshl_add_u64 v[218:219], s[20:21], 0, v[164:165]
	ds_read_b128 v[174:177], v203 offset:32768
	ds_read_b128 v[178:181], v203 offset:33792
	ds_read_b128 v[182:185], v203 offset:34816
	ds_read_b128 v[186:189], v203 offset:35840
	ds_read_b128 v[190:193], v203 offset:36864
	ds_read_b128 v[194:197], v203 offset:37888
	ds_read_b128 v[204:207], v203 offset:38912
	ds_read_b128 v[208:211], v203 offset:39936
	global_load_lds_dwordx4 v[218:219], off
	v_lshl_add_u64 v[218:219], s[20:21], 0, v[166:167]
	s_mov_b32 m0, s31
	s_nop 0
	global_load_lds_dwordx4 v[218:219], off
	s_waitcnt vmcnt(8)
	s_waitcnt lgkmcnt(0)
	s_barrier
	s_setprio 1
	s_waitcnt lgkmcnt(0)
	v_mfma_f32_16x16x32_bf16 v[56:59], v[68:71], v[174:177], v[56:59]
	v_mfma_f32_16x16x32_bf16 v[52:55], v[76:79], v[174:177], v[52:55]
	v_mfma_f32_16x16x32_bf16 v[88:91], v[68:71], v[182:185], v[88:91]
	v_mfma_f32_16x16x32_bf16 v[84:87], v[76:79], v[182:185], v[84:87]
	v_mfma_f32_16x16x32_bf16 v[120:123], v[68:71], v[190:193], v[120:123]
	v_mfma_f32_16x16x32_bf16 v[116:119], v[76:79], v[190:193], v[116:119]
	v_mfma_f32_16x16x32_bf16 v[128:131], v[68:71], v[204:207], v[128:131]
	v_mfma_f32_16x16x32_bf16 v[124:127], v[76:79], v[204:207], v[124:127]
	v_mfma_f32_16x16x32_bf16 v[56:59], v[72:75], v[178:181], v[56:59]
	v_mfma_f32_16x16x32_bf16 v[52:55], v[80:83], v[178:181], v[52:55]
	v_mfma_f32_16x16x32_bf16 v[88:91], v[72:75], v[186:189], v[88:91]
	v_mfma_f32_16x16x32_bf16 v[84:87], v[80:83], v[186:189], v[84:87]
	v_mfma_f32_16x16x32_bf16 v[120:123], v[72:75], v[194:197], v[120:123]
	v_mfma_f32_16x16x32_bf16 v[116:119], v[80:83], v[194:197], v[116:119]
	v_mfma_f32_16x16x32_bf16 v[128:131], v[72:75], v[208:211], v[128:131]
	v_mfma_f32_16x16x32_bf16 v[124:127], v[80:83], v[208:211], v[124:127]
	s_setprio 0
	s_setprio 1
	v_mfma_f32_16x16x32_bf16 v[160:163], v[100:103], v[174:177], v[160:163]
	v_mfma_f32_16x16x32_bf16 v[156:159], v[132:135], v[174:177], v[156:159]
	v_mfma_f32_16x16x32_bf16 v[152:155], v[100:103], v[182:185], v[152:155]
	v_mfma_f32_16x16x32_bf16 v[148:151], v[132:135], v[182:185], v[148:151]
	v_mfma_f32_16x16x32_bf16 v[144:147], v[100:103], v[190:193], v[144:147]
	v_mfma_f32_16x16x32_bf16 v[140:143], v[132:135], v[190:193], v[140:143]
	v_mfma_f32_16x16x32_bf16 v[112:115], v[100:103], v[204:207], v[112:115]
	v_mfma_f32_16x16x32_bf16 v[108:111], v[132:135], v[204:207], v[108:111]
	v_mfma_f32_16x16x32_bf16 v[160:163], v[104:107], v[178:181], v[160:163]
	v_mfma_f32_16x16x32_bf16 v[156:159], v[136:139], v[178:181], v[156:159]
	v_mfma_f32_16x16x32_bf16 v[152:155], v[104:107], v[186:189], v[152:155]
	v_mfma_f32_16x16x32_bf16 v[148:151], v[136:139], v[186:189], v[148:151]
	v_mfma_f32_16x16x32_bf16 v[144:147], v[104:107], v[194:197], v[144:147]
	v_mfma_f32_16x16x32_bf16 v[140:143], v[136:139], v[194:197], v[140:143]
	v_mfma_f32_16x16x32_bf16 v[112:115], v[104:107], v[208:211], v[112:115]
	v_mfma_f32_16x16x32_bf16 v[108:111], v[136:139], v[208:211], v[108:111]
	s_setprio 0
	s_barrier
; #define MG_LOAD(c, buf) do { _Pragma("unroll") for (int m2 = 0; m2 < 2; ++m2) _Pragma("unroll") for (int bj = 0; bj < 2; ++bj) { \
;             const size_t ro = (size_t)(row0 + ((c) >> 1) * HALF + (2 * ((c) & 1) + m2) * 16) * DM + col0 + bj * HALF; ga[buf][m2][bj] = *(const u32x2*)(GAx + (ro & amask)); gb[buf][m2][bj] = *(const u32x2*)(GB + ro); } } while (0)
; #define PG8_STAGE(bufoff, gbase, voff) do { _Pragma("unroll") for (int _i = 0; _i < 2; ++_i) \
;         __builtin_amdgcn_global_load_lds((const unsigned*)((const char*)(gbase) + (voff)[_i]), (PG8_LAS unsigned*)(lds + (bufoff) + ldsw + _i * 8192), 16, 0, 0); } while (0)
; #define PG8_LDA(dst, b, h) do { _Pragma("unroll") for (int m = 0; m < 4; ++m) _Pragma("unroll") for (int k = 0; k < 2; ++k) dst[m][k] = *(const PG8_LAS bf16x8*)(lds + PG8_SA(b, h) + aoff + m * 2048 + k * 1024); } while (0)
; #define PG8_MMA(ai, bj, At, Bt) do { __builtin_amdgcn_s_setprio(1); _Pragma("unroll") for (int m = 0; m < 4; ++m) _Pragma("unroll") for (int n = 0; n < 2; ++n) _Pragma("unroll") for (int k = 0; k < 2; ++k) \
;         acc[ai][bj][m][n] = __builtin_amdgcn_mfma_f32_16x16x32_bf16(Bt[n][k], At[m][k], acc[ai][bj][m][n], 0, 0, 0); __builtin_amdgcn_s_setprio(0); } while (0)
; #define PG8_WAIT_V(n) asm volatile("s_waitcnt vmcnt(" #n ")" ::: "memory")
; #define PG8_WAIT_L(n) asm volatile("s_waitcnt lgkmcnt(" #n ")" ::: "memory")
; #define PG8_BAR __builtin_amdgcn_s_barrier()
; #define PG8_SCHED __builtin_amdgcn_sched_barrier(0)
;     __device__ __forceinline__ void operator()(f32x4 (&acc)[2][2][4][2], const Unit& u, int wr, int wc, int fr, int fq) const {
;     ...
;         MG_LOAD(0, 0); MG_LOAD(1, 1);
; template <class Epi, class Sched, bool ALIGN_EPI = false, bool SP2 = false>
; __device__ __forceinline__ void gemm_phase(PG8_LAS unsigned char* lds, const Gemm g, const Sched& S, const Epi& E) {
;     ...
;             PG8_LDA(At, 1, 1); PG8_STAGE(PG8_SB(1, 0), b3, voffB); PG8_STAGE(PG8_SB(1, 1), b3 + hstep, voffB); PG8_STAGE(PG8_SA(1, 0), a3, voffA);
;             PG8_WAIT_V(8); PG8_WAIT_L(0); PG8_BAR; if (cur.half == 0) { PG8_MMA(1, 0, At, B0); PG8_MMA(1, 1, At, B1); } PG8_BAR; PG8_SCHED;
	s_add_i32 s20, s65, s27
	v_lshl_add_u64 v[198:199], v[198:199], 0, s[42:43]
	s_mov_b32 m0, s20
	ds_read_b128 v[174:177], v203 offset:49152
	ds_read_b128 v[178:181], v203 offset:50176
	ds_read_b128 v[182:185], v203 offset:51200
	ds_read_b128 v[186:189], v203 offset:52224
	ds_read_b128 v[190:193], v203 offset:53248
	ds_read_b128 v[194:197], v203 offset:54272
	ds_read_b128 v[204:207], v203 offset:55296
	ds_read_b128 v[208:211], v203 offset:56320
	global_load_lds_dwordx4 v[198:199], off
	s_add_i32 m0, s20, 0x2000
	s_add_u32 s14, s14, 0x20080
	v_lshl_add_u64 v[198:199], v[212:213], 0, s[42:43]
	s_addc_u32 s15, s15, 0
	s_add_i32 s20, s66, s27
	global_load_lds_dwordx4 v[198:199], off
	v_lshl_add_u64 v[198:199], s[14:15], 0, v[2:3]
	s_mov_b32 m0, s20
	s_nop 0
	global_load_lds_dwordx4 v[198:199], off
	v_lshl_add_u64 v[198:199], s[14:15], 0, v[168:169]
	s_add_i32 m0, s20, 0x2000
	s_nop 0
	global_load_lds_dwordx4 v[198:199], off
	v_lshl_add_u64 v[198:199], v[214:215], 0, s[42:43]
	s_mov_b32 m0, s36
	s_nop 0
	global_load_lds_dwordx4 v[198:199], off
	v_lshl_add_u64 v[198:199], v[216:217], 0, s[42:43]
	s_mov_b32 m0, s40
	s_nop 0
	global_load_lds_dwordx4 v[198:199], off
	s_waitcnt vmcnt(8)
	s_cmp_lg_u32 s64, 4
	s_cbranch_scc1 .Lmg_nopf
	s_lshl_b32 s20, s4, 8
	s_lshl_b32 s21, s0, 8
	s_cmp_gt_i32 s0, 3
	s_cbranch_scc1 .Lmg_pf2
	v_add_u32_e32 v253, s20, v200
	v_or_b32_e32 v252, s21, v202
	v_lshl_add_u32 v252, v253, 10, v252
	global_load_dwordx2 v[228:229], v252, s[10:11]
	global_load_dwordx2 v[232:233], v252, s[34:35]
	global_load_dwordx2 v[230:231], v252, s[10:11] offset:128
	global_load_dwordx2 v[234:235], v252, s[34:35] offset:128
	v_add_u32_e32 v252, 0x4000, v252
	global_load_dwordx2 v[236:237], v252, s[10:11]
	global_load_dwordx2 v[240:241], v252, s[34:35]
	global_load_dwordx2 v[238:239], v252, s[10:11] offset:128
	global_load_dwordx2 v[242:243], v252, s[34:35] offset:128
	v_add_u32_e32 v252, 0x4000, v252
	global_load_dwordx2 v[244:245], v252, s[10:11]
	global_load_dwordx2 v[248:249], v252, s[34:35]
	global_load_dwordx2 v[246:247], v252, s[10:11] offset:128
	global_load_dwordx2 v[250:251], v252, s[34:35] offset:128
	s_branch .Lmg_nopf
.Lmg_pf2:
	s_add_i32 s20, s20, 0xffffc000
	s_add_i32 s21, s21, 0xfffffc00
	v_add_u32_e32 v253, s20, v200
	v_or_b32_e32 v252, s21, v202
	v_lshl_add_u32 v252, v253, 10, v252
	v_lshlrev_b32_e32 v253, 1, v252
	global_load_dwordx2 v[228:229], v252, s[10:11]
	global_load_dwordx2 v[230:231], v252, s[10:11] offset:128
	v_add_u32_e32 v252, 0x4000, v252
	global_load_dwordx2 v[232:233], v252, s[10:11]
	global_load_dwordx2 v[234:235], v252, s[10:11] offset:128
	v_add_u32_e32 v252, 0x4000, v252
	global_load_dwordx2 v[236:237], v252, s[10:11]
	global_load_dwordx2 v[238:239], v252, s[10:11] offset:128
	v_add_u32_e32 v252, 0x4000, v252
	global_load_dwordx2 v[240:241], v252, s[10:11]
	global_load_dwordx2 v[242:243], v252, s[10:11] offset:128
	v_add_u32_e32 v252, 0x14000, v252
	global_load_dwordx2 v[244:245], v252, s[10:11]
	global_load_dwordx2 v[246:247], v252, s[10:11] offset:128
	v_add_u32_e32 v252, 0x4000, v252
	global_load_dwordx2 v[248:249], v252, s[10:11]
	global_load_dwordx2 v[250:251], v252, s[10:11] offset:128
.Lmg_nopf:
	s_waitcnt lgkmcnt(0)
	s_barrier
	s_setprio 1
	s_waitcnt lgkmcnt(0)
	v_mfma_f32_16x16x32_bf16 v[96:99], v[68:71], v[174:177], v[96:99]
	v_mfma_f32_16x16x32_bf16 v[92:95], v[76:79], v[174:177], v[92:95]
	v_mfma_f32_16x16x32_bf16 v[64:67], v[68:71], v[182:185], v[64:67]
	v_mfma_f32_16x16x32_bf16 v[60:63], v[76:79], v[182:185], v[60:63]
	v_mfma_f32_16x16x32_bf16 v[32:35], v[68:71], v[190:193], v[32:35]
	v_mfma_f32_16x16x32_bf16 v[28:31], v[76:79], v[190:193], v[28:31]
	v_mfma_f32_16x16x32_bf16 v[16:19], v[68:71], v[204:207], v[16:19]
	v_mfma_f32_16x16x32_bf16 v[12:15], v[76:79], v[204:207], v[12:15]
	v_mfma_f32_16x16x32_bf16 v[96:99], v[72:75], v[178:181], v[96:99]
	v_mfma_f32_16x16x32_bf16 v[92:95], v[80:83], v[178:181], v[92:95]
	v_mfma_f32_16x16x32_bf16 v[64:67], v[72:75], v[186:189], v[64:67]
	v_mfma_f32_16x16x32_bf16 v[60:63], v[80:83], v[186:189], v[60:63]
	v_mfma_f32_16x16x32_bf16 v[32:35], v[72:75], v[194:197], v[32:35]
	v_mfma_f32_16x16x32_bf16 v[28:31], v[80:83], v[194:197], v[28:31]
	v_mfma_f32_16x16x32_bf16 v[16:19], v[72:75], v[208:211], v[16:19]
	v_mfma_f32_16x16x32_bf16 v[12:15], v[80:83], v[208:211], v[12:15]
	s_setprio 0
	s_setprio 1
	v_mfma_f32_16x16x32_bf16 v[36:39], v[100:103], v[174:177], v[36:39]
	v_mfma_f32_16x16x32_bf16 v[80:83], v[104:107], v[178:181], v[36:39]
	v_mfma_f32_16x16x32_bf16 v[36:39], v[132:135], v[174:177], v[40:43]
	v_mfma_f32_16x16x32_bf16 v[76:79], v[136:139], v[178:181], v[36:39]
	v_mfma_f32_16x16x32_bf16 v[36:39], v[100:103], v[182:185], v[48:51]
	v_mfma_f32_16x16x32_bf16 v[48:51], v[104:107], v[186:189], v[36:39]
	v_mfma_f32_16x16x32_bf16 v[36:39], v[132:135], v[182:185], v[44:47]
	v_mfma_f32_16x16x32_bf16 v[24:27], v[100:103], v[190:193], v[24:27]
	v_mfma_f32_16x16x32_bf16 v[20:23], v[132:135], v[190:193], v[20:23]
	v_mfma_f32_16x16x32_bf16 v[8:11], v[100:103], v[204:207], v[8:11]
	v_mfma_f32_16x16x32_bf16 v[4:7], v[132:135], v[204:207], v[4:7]
	v_mfma_f32_16x16x32_bf16 v[44:47], v[136:139], v[186:189], v[36:39]
	v_mfma_f32_16x16x32_bf16 v[24:27], v[104:107], v[194:197], v[24:27]
	v_mfma_f32_16x16x32_bf16 v[20:23], v[136:139], v[194:197], v[20:23]
	v_mfma_f32_16x16x32_bf16 v[8:11], v[104:107], v[208:211], v[8:11]
	v_mfma_f32_16x16x32_bf16 v[4:7], v[136:139], v[208:211], v[4:7]
	s_setprio 0
	s_barrier
	s_add_i32 s64, s64, 2
	s_add_u32 s6, s6, 0x100
	s_addc_u32 s7, s7, 0
	s_add_u32 s62, s62, 0x100
	s_addc_u32 s63, s63, 0
	s_cmp_gt_u32 s64, 5
	s_cbranch_scc0 .LBB0_1135
	s_and_b64 vcc, exec, s[16:17]
	s_cbranch_vccz .LBB0_1138
	s_barrier
; __device__ __forceinline__ u32x4 pack8(const f32x4 a, const f32x4 b) { u32x4 w; w.x = cvt_pk_bf16(a[0], a[1]); w.y = cvt_pk_bf16(a[2], a[3]); w.z = cvt_pk_bf16(b[0], b[1]); w.w = cvt_pk_bf16(b[2], b[3]); return w; }
;     __device__ __forceinline__ void operator()(f32x4 (&acc)[2][2][4][2], const Unit& u, int wr, int wc, int fr, int fq) const {
;     ...
;         MG_LOAD(0, 0); MG_LOAD(1, 1);
;         asm volatile("" ::: "memory");
; #pragma unroll
;         for (int c = 0; c < 4; ++c) { const int ai = c >> 1;
; #pragma unroll
;             for (int m2 = 0; m2 < 2; ++m2) { const int m = 2 * (c & 1) + m2;
; #pragma unroll
;                 for (int bj = 0; bj < 2; ++bj) { const u32x2 a2 = ga[c & 1][m2][bj], b2 = gb[c & 1][m2][bj]; const float q = 1.0f / 255.0f;
;                     const f32x4 sa0 = {(float)((a2.x >> 0) & 0xffu), (float)((a2.x >> 8) & 0xffu), (float)((a2.x >> 16) & 0xffu), (float)((a2.x >> 24) & 0xffu)};
;                     const f32x4 sa1 = {(float)((a2.y >> 0) & 0xffu), (float)((a2.y >> 8) & 0xffu), (float)((a2.y >> 16) & 0xffu), (float)((a2.y >> 24) & 0xffu)};
;                     f32x4 sb0 = {(float)((b2.x >> 0) & 0xffu), (float)((b2.x >> 8) & 0xffu), (float)((b2.x >> 16) & 0xffu), (float)((b2.x >> 24) & 0xffu)};
;                     f32x4 sb1 = {(float)((b2.y >> 0) & 0xffu), (float)((b2.y >> 8) & 0xffu), (float)((b2.y >> 16) & 0xffu), (float)((b2.y >> 24) & 0xffu)};
; #pragma unroll
;                     for (int e = 0; e < 4; ++e) { sb0[e] = fmaxf(sb0[e], 2.55e-4f); sb1[e] = fmaxf(sb1[e], 2.55e-4f); }
;                     if (second) *(u32x4*)(MERGED + (size_t)(row0 + ai * HALF + m * 16) * DM + col0 + bj * HALF) = pack8(acc[ai][bj][m][0] * (sb0 * q), acc[ai][bj][m][1] * (sb1 * q));
;                     if (!second) { f32x4 r0, r1;
; #pragma unroll
;                         for (int e = 0; e < 4; ++e) { r0[e] = sa0[e] * __builtin_amdgcn_rcpf(sb0[e]); r1[e] = sa1[e] * __builtin_amdgcn_rcpf(sb1[e]); }
;                         acc[ai][bj][m][0] = acc[ai][bj][m][0] * r0; acc[ai][bj][m][1] = acc[ai][bj][m][1] * r1; }
.LBB0_1138:
	s_cmp_gt_i32 s0, 3
	s_cbranch_scc1 .Lmg_second
	v_add_u32_e32 v252, 0x4000, v252
	global_load_dwordx2 v[36:37], v252, s[10:11]
	global_load_dwordx2 v[40:41], v252, s[34:35]
	global_load_dwordx2 v[38:39], v252, s[10:11] offset:128
	global_load_dwordx2 v[42:43], v252, s[34:35] offset:128
	v_add_u32_e32 v252, 0x14000, v252
	global_load_dwordx2 v[68:69], v252, s[10:11]
	global_load_dwordx2 v[72:73], v252, s[34:35]
	global_load_dwordx2 v[70:71], v252, s[10:11] offset:128
	global_load_dwordx2 v[74:75], v252, s[34:35] offset:128
	v_add_u32_e32 v252, 0x4000, v252
	global_load_dwordx2 v[100:101], v252, s[10:11]
	global_load_dwordx2 v[104:105], v252, s[34:35]
	global_load_dwordx2 v[102:103], v252, s[10:11] offset:128
	global_load_dwordx2 v[106:107], v252, s[34:35] offset:128
	v_add_u32_e32 v252, 0x4000, v252
	global_load_dwordx2 v[132:133], v252, s[10:11]
	global_load_dwordx2 v[136:137], v252, s[34:35]
	global_load_dwordx2 v[134:135], v252, s[10:11] offset:128
	global_load_dwordx2 v[138:139], v252, s[34:35] offset:128
	v_add_u32_e32 v252, 0x4000, v252
	global_load_dwordx2 v[174:175], v252, s[10:11]
	global_load_dwordx2 v[178:179], v252, s[34:35]
	global_load_dwordx2 v[176:177], v252, s[10:11] offset:128
	global_load_dwordx2 v[180:181], v252, s[34:35] offset:128
	s_waitcnt vmcnt(30)
	v_cvt_f32_ubyte0_e32 v212, v228
	v_cvt_f32_ubyte1_e32 v213, v228
	v_cvt_f32_ubyte2_e32 v214, v228
	v_cvt_f32_ubyte3_e32 v215, v228
	v_cvt_f32_ubyte0_e32 v216, v229
	v_cvt_f32_ubyte1_e32 v217, v229
	v_cvt_f32_ubyte2_e32 v218, v229
	v_cvt_f32_ubyte3_e32 v219, v229
	v_max_f32_e32 v212, 0x3985b185, v212
	v_max_f32_e32 v213, 0x3985b185, v213
	v_max_f32_e32 v214, 0x3985b185, v214
	v_max_f32_e32 v215, 0x3985b185, v215
	v_max_f32_e32 v216, 0x3985b185, v216
	v_max_f32_e32 v217, 0x3985b185, v217
	v_max_f32_e32 v218, 0x3985b185, v218
	v_max_f32_e32 v219, 0x3985b185, v219
	v_rcp_f32_e32 v212, v212
	v_rcp_f32_e32 v213, v213
	v_rcp_f32_e32 v214, v214
	v_rcp_f32_e32 v215, v215
	v_rcp_f32_e32 v216, v216
	v_rcp_f32_e32 v217, v217
	v_rcp_f32_e32 v218, v218
	v_rcp_f32_e32 v219, v219
	v_cvt_f32_ubyte0_e32 v204, v232
	v_cvt_f32_ubyte1_e32 v205, v232
	v_cvt_f32_ubyte2_e32 v206, v232
	v_cvt_f32_ubyte3_e32 v207, v232
	v_cvt_f32_ubyte0_e32 v208, v233
	v_cvt_f32_ubyte1_e32 v209, v233
	v_cvt_f32_ubyte2_e32 v210, v233
	v_cvt_f32_ubyte3_e32 v211, v233
	v_pk_mul_f32 v[212:213], v[212:213], v[204:205]
	v_pk_mul_f32 v[214:215], v[214:215], v[206:207]
	v_pk_mul_f32 v[216:217], v[216:217], v[208:209]
	v_pk_mul_f32 v[218:219], v[218:219], v[210:211]
	v_pk_mul_f32 v[56:57], v[56:57], v[212:213]
	v_pk_mul_f32 v[58:59], v[58:59], v[214:215]
	v_pk_mul_f32 v[52:53], v[52:53], v[216:217]
	v_pk_mul_f32 v[54:55], v[54:55], v[218:219]
	s_waitcnt vmcnt(28)
	v_cvt_f32_ubyte0_e32 v212, v230
	v_cvt_f32_ubyte1_e32 v213, v230
	v_cvt_f32_ubyte2_e32 v214, v230
	v_cvt_f32_ubyte3_e32 v215, v230
	v_cvt_f32_ubyte0_e32 v216, v231
	v_cvt_f32_ubyte1_e32 v217, v231
	v_cvt_f32_ubyte2_e32 v218, v231
	v_cvt_f32_ubyte3_e32 v219, v231
	v_max_f32_e32 v212, 0x3985b185, v212
	v_max_f32_e32 v213, 0x3985b185, v213
	v_max_f32_e32 v214, 0x3985b185, v214
	v_max_f32_e32 v215, 0x3985b185, v215
	v_max_f32_e32 v216, 0x3985b185, v216
	v_max_f32_e32 v217, 0x3985b185, v217
	v_max_f32_e32 v218, 0x3985b185, v218
	v_max_f32_e32 v219, 0x3985b185, v219
	v_rcp_f32_e32 v212, v212
	v_rcp_f32_e32 v213, v213
	v_rcp_f32_e32 v214, v214
	v_rcp_f32_e32 v215, v215
	v_rcp_f32_e32 v216, v216
	v_rcp_f32_e32 v217, v217
	v_rcp_f32_e32 v218, v218
	v_rcp_f32_e32 v219, v219
	v_cvt_f32_ubyte0_e32 v204, v234
	v_cvt_f32_ubyte1_e32 v205, v234
	v_cvt_f32_ubyte2_e32 v206, v234
	v_cvt_f32_ubyte3_e32 v207, v234
	v_cvt_f32_ubyte0_e32 v208, v235
	v_cvt_f32_ubyte1_e32 v209, v235
	v_cvt_f32_ubyte2_e32 v210, v235
	v_cvt_f32_ubyte3_e32 v211, v235
	v_pk_mul_f32 v[212:213], v[212:213], v[204:205]
	v_pk_mul_f32 v[214:215], v[214:215], v[206:207]
	v_pk_mul_f32 v[216:217], v[216:217], v[208:209]
	v_pk_mul_f32 v[218:219], v[218:219], v[210:211]
	v_pk_mul_f32 v[160:161], v[160:161], v[212:213]
	v_pk_mul_f32 v[162:163], v[162:163], v[214:215]
	v_pk_mul_f32 v[156:157], v[156:157], v[216:217]
	v_pk_mul_f32 v[158:159], v[158:159], v[218:219]
	s_waitcnt vmcnt(26)
	v_cvt_f32_ubyte0_e32 v212, v236
	v_cvt_f32_ubyte1_e32 v213, v236
	v_cvt_f32_ubyte2_e32 v214, v236
	v_cvt_f32_ubyte3_e32 v215, v236
	v_cvt_f32_ubyte0_e32 v216, v237
	v_cvt_f32_ubyte1_e32 v217, v237
	v_cvt_f32_ubyte2_e32 v218, v237
	v_cvt_f32_ubyte3_e32 v219, v237
	v_max_f32_e32 v212, 0x3985b185, v212
	v_max_f32_e32 v213, 0x3985b185, v213
	v_max_f32_e32 v214, 0x3985b185, v214
	v_max_f32_e32 v215, 0x3985b185, v215
	v_max_f32_e32 v216, 0x3985b185, v216
	v_max_f32_e32 v217, 0x3985b185, v217
	v_max_f32_e32 v218, 0x3985b185, v218
	v_max_f32_e32 v219, 0x3985b185, v219
	v_rcp_f32_e32 v212, v212
	v_rcp_f32_e32 v213, v213
	v_rcp_f32_e32 v214, v214
	v_rcp_f32_e32 v215, v215
	v_rcp_f32_e32 v216, v216
	v_rcp_f32_e32 v217, v217
	v_rcp_f32_e32 v218, v218
	v_rcp_f32_e32 v219, v219
	v_cvt_f32_ubyte0_e32 v204, v240
	v_cvt_f32_ubyte1_e32 v205, v240
	v_cvt_f32_ubyte2_e32 v206, v240
	v_cvt_f32_ubyte3_e32 v207, v240
	v_cvt_f32_ubyte0_e32 v208, v241
	v_cvt_f32_ubyte1_e32 v209, v241
	v_cvt_f32_ubyte2_e32 v210, v241
	v_cvt_f32_ubyte3_e32 v211, v241
	v_pk_mul_f32 v[212:213], v[212:213], v[204:205]
	v_pk_mul_f32 v[214:215], v[214:215], v[206:207]
	v_pk_mul_f32 v[216:217], v[216:217], v[208:209]
	v_pk_mul_f32 v[218:219], v[218:219], v[210:211]
	v_pk_mul_f32 v[88:89], v[88:89], v[212:213]
	v_pk_mul_f32 v[90:91], v[90:91], v[214:215]
	v_pk_mul_f32 v[84:85], v[84:85], v[216:217]
	v_pk_mul_f32 v[86:87], v[86:87], v[218:219]
	s_waitcnt vmcnt(24)
; __device__ __forceinline__ u32x4 pack8(const f32x4 a, const f32x4 b) { u32x4 w; w.x = cvt_pk_bf16(a[0], a[1]); w.y = cvt_pk_bf16(a[2], a[3]); w.z = cvt_pk_bf16(b[0], b[1]); w.w = cvt_pk_bf16(b[2], b[3]); return w; }
;     __device__ __forceinline__ void operator()(f32x4 (&acc)[2][2][4][2], const Unit& u, int wr, int wc, int fr, int fq) const {
;     ...
;                 for (int bj = 0; bj < 2; ++bj) { const u32x2 a2 = ga[c & 1][m2][bj], b2 = gb[c & 1][m2][bj]; const float q = 1.0f / 255.0f;
;                     const f32x4 sa0 = {(float)((a2.x >> 0) & 0xffu), (float)((a2.x >> 8) & 0xffu), (float)((a2.x >> 16) & 0xffu), (float)((a2.x >> 24) & 0xffu)};
;                     const f32x4 sa1 = {(float)((a2.y >> 0) & 0xffu), (float)((a2.y >> 8) & 0xffu), (float)((a2.y >> 16) & 0xffu), (float)((a2.y >> 24) & 0xffu)};
;                     f32x4 sb0 = {(float)((b2.x >> 0) & 0xffu), (float)((b2.x >> 8) & 0xffu), (float)((b2.x >> 16) & 0xffu), (float)((b2.x >> 24) & 0xffu)};
;                     f32x4 sb1 = {(float)((b2.y >> 0) & 0xffu), (float)((b2.y >> 8) & 0xffu), (float)((b2.y >> 16) & 0xffu), (float)((b2.y >> 24) & 0xffu)};
; #pragma unroll
;                     for (int e = 0; e < 4; ++e) { sb0[e] = fmaxf(sb0[e], 2.55e-4f); sb1[e] = fmaxf(sb1[e], 2.55e-4f); }
;                     if (second) *(u32x4*)(MERGED + (size_t)(row0 + ai * HALF + m * 16) * DM + col0 + bj * HALF) = pack8(acc[ai][bj][m][0] * (sb0 * q), acc[ai][bj][m][1] * (sb1 * q));
;                     if (!second) { f32x4 r0, r1;
; #pragma unroll
;                         for (int e = 0; e < 4; ++e) { r0[e] = sa0[e] * __builtin_amdgcn_rcpf(sb0[e]); r1[e] = sa1[e] * __builtin_amdgcn_rcpf(sb1[e]); }
;                         acc[ai][bj][m][0] = acc[ai][bj][m][0] * r0; acc[ai][bj][m][1] = acc[ai][bj][m][1] * r1; }
	v_cvt_f32_ubyte0_e32 v212, v238
	v_cvt_f32_ubyte1_e32 v213, v238
	v_cvt_f32_ubyte2_e32 v214, v238
	v_cvt_f32_ubyte3_e32 v215, v238
	v_cvt_f32_ubyte0_e32 v216, v239
	v_cvt_f32_ubyte1_e32 v217, v239
	v_cvt_f32_ubyte2_e32 v218, v239
	v_cvt_f32_ubyte3_e32 v219, v239
	v_max_f32_e32 v212, 0x3985b185, v212
	v_max_f32_e32 v213, 0x3985b185, v213
	v_max_f32_e32 v214, 0x3985b185, v214
	v_max_f32_e32 v215, 0x3985b185, v215
	v_max_f32_e32 v216, 0x3985b185, v216
	v_max_f32_e32 v217, 0x3985b185, v217
	v_max_f32_e32 v218, 0x3985b185, v218
	v_max_f32_e32 v219, 0x3985b185, v219
	v_rcp_f32_e32 v212, v212
	v_rcp_f32_e32 v213, v213
	v_rcp_f32_e32 v214, v214
	v_rcp_f32_e32 v215, v215
	v_rcp_f32_e32 v216, v216
	v_rcp_f32_e32 v217, v217
	v_rcp_f32_e32 v218, v218
	v_rcp_f32_e32 v219, v219
	v_cvt_f32_ubyte0_e32 v204, v242
	v_cvt_f32_ubyte1_e32 v205, v242
	v_cvt_f32_ubyte2_e32 v206, v242
	v_cvt_f32_ubyte3_e32 v207, v242
	v_cvt_f32_ubyte0_e32 v208, v243
	v_cvt_f32_ubyte1_e32 v209, v243
	v_cvt_f32_ubyte2_e32 v210, v243
	v_cvt_f32_ubyte3_e32 v211, v243
	v_pk_mul_f32 v[212:213], v[212:213], v[204:205]
	v_pk_mul_f32 v[214:215], v[214:215], v[206:207]
	v_pk_mul_f32 v[216:217], v[216:217], v[208:209]
	v_pk_mul_f32 v[218:219], v[218:219], v[210:211]
	v_pk_mul_f32 v[152:153], v[152:153], v[212:213]
	v_pk_mul_f32 v[154:155], v[154:155], v[214:215]
	v_pk_mul_f32 v[148:149], v[148:149], v[216:217]
	v_pk_mul_f32 v[150:151], v[150:151], v[218:219]
	s_waitcnt vmcnt(22)
	v_cvt_f32_ubyte0_e32 v212, v244
	v_cvt_f32_ubyte1_e32 v213, v244
	v_cvt_f32_ubyte2_e32 v214, v244
	v_cvt_f32_ubyte3_e32 v215, v244
	v_cvt_f32_ubyte0_e32 v216, v245
	v_cvt_f32_ubyte1_e32 v217, v245
	v_cvt_f32_ubyte2_e32 v218, v245
	v_cvt_f32_ubyte3_e32 v219, v245
	v_max_f32_e32 v212, 0x3985b185, v212
	v_max_f32_e32 v213, 0x3985b185, v213
	v_max_f32_e32 v214, 0x3985b185, v214
	v_max_f32_e32 v215, 0x3985b185, v215
	v_max_f32_e32 v216, 0x3985b185, v216
	v_max_f32_e32 v217, 0x3985b185, v217
	v_max_f32_e32 v218, 0x3985b185, v218
	v_max_f32_e32 v219, 0x3985b185, v219
	v_rcp_f32_e32 v212, v212
	v_rcp_f32_e32 v213, v213
	v_rcp_f32_e32 v214, v214
	v_rcp_f32_e32 v215, v215
	v_rcp_f32_e32 v216, v216
	v_rcp_f32_e32 v217, v217
	v_rcp_f32_e32 v218, v218
	v_rcp_f32_e32 v219, v219
	v_cvt_f32_ubyte0_e32 v204, v248
	v_cvt_f32_ubyte1_e32 v205, v248
	v_cvt_f32_ubyte2_e32 v206, v248
	v_cvt_f32_ubyte3_e32 v207, v248
	v_cvt_f32_ubyte0_e32 v208, v249
	v_cvt_f32_ubyte1_e32 v209, v249
	v_cvt_f32_ubyte2_e32 v210, v249
	v_cvt_f32_ubyte3_e32 v211, v249
	v_pk_mul_f32 v[212:213], v[212:213], v[204:205]
	v_pk_mul_f32 v[214:215], v[214:215], v[206:207]
	v_pk_mul_f32 v[216:217], v[216:217], v[208:209]
	v_pk_mul_f32 v[218:219], v[218:219], v[210:211]
	v_pk_mul_f32 v[120:121], v[120:121], v[212:213]
	v_pk_mul_f32 v[122:123], v[122:123], v[214:215]
	v_pk_mul_f32 v[116:117], v[116:117], v[216:217]
	v_pk_mul_f32 v[118:119], v[118:119], v[218:219]
	s_waitcnt vmcnt(20)
	v_cvt_f32_ubyte0_e32 v212, v246
	v_cvt_f32_ubyte1_e32 v213, v246
	v_cvt_f32_ubyte2_e32 v214, v246
	v_cvt_f32_ubyte3_e32 v215, v246
	v_cvt_f32_ubyte0_e32 v216, v247
	v_cvt_f32_ubyte1_e32 v217, v247
	v_cvt_f32_ubyte2_e32 v218, v247
	v_cvt_f32_ubyte3_e32 v219, v247
	v_max_f32_e32 v212, 0x3985b185, v212
	v_max_f32_e32 v213, 0x3985b185, v213
	v_max_f32_e32 v214, 0x3985b185, v214
	v_max_f32_e32 v215, 0x3985b185, v215
	v_max_f32_e32 v216, 0x3985b185, v216
	v_max_f32_e32 v217, 0x3985b185, v217
	v_max_f32_e32 v218, 0x3985b185, v218
	v_max_f32_e32 v219, 0x3985b185, v219
	v_rcp_f32_e32 v212, v212
	v_rcp_f32_e32 v213, v213
	v_rcp_f32_e32 v214, v214
	v_rcp_f32_e32 v215, v215
	v_rcp_f32_e32 v216, v216
	v_rcp_f32_e32 v217, v217
	v_rcp_f32_e32 v218, v218
	v_rcp_f32_e32 v219, v219
	v_cvt_f32_ubyte0_e32 v204, v250
	v_cvt_f32_ubyte1_e32 v205, v250
	v_cvt_f32_ubyte2_e32 v206, v250
	v_cvt_f32_ubyte3_e32 v207, v250
	v_cvt_f32_ubyte0_e32 v208, v251
	v_cvt_f32_ubyte1_e32 v209, v251
	v_cvt_f32_ubyte2_e32 v210, v251
	v_cvt_f32_ubyte3_e32 v211, v251
	v_pk_mul_f32 v[212:213], v[212:213], v[204:205]
	v_pk_mul_f32 v[214:215], v[214:215], v[206:207]
	v_pk_mul_f32 v[216:217], v[216:217], v[208:209]
	v_pk_mul_f32 v[218:219], v[218:219], v[210:211]
	v_pk_mul_f32 v[144:145], v[144:145], v[212:213]
	v_pk_mul_f32 v[146:147], v[146:147], v[214:215]
	v_pk_mul_f32 v[140:141], v[140:141], v[216:217]
	v_pk_mul_f32 v[142:143], v[142:143], v[218:219]
	s_waitcnt vmcnt(18)
	v_cvt_f32_ubyte0_e32 v212, v36
	v_cvt_f32_ubyte1_e32 v213, v36
	v_cvt_f32_ubyte2_e32 v214, v36
	v_cvt_f32_ubyte3_e32 v215, v36
	v_cvt_f32_ubyte0_e32 v216, v37
	v_cvt_f32_ubyte1_e32 v217, v37
	v_cvt_f32_ubyte2_e32 v218, v37
	v_cvt_f32_ubyte3_e32 v219, v37
	v_max_f32_e32 v212, 0x3985b185, v212
	v_max_f32_e32 v213, 0x3985b185, v213
	v_max_f32_e32 v214, 0x3985b185, v214
	v_max_f32_e32 v215, 0x3985b185, v215
	v_max_f32_e32 v216, 0x3985b185, v216
	v_max_f32_e32 v217, 0x3985b185, v217
	v_max_f32_e32 v218, 0x3985b185, v218
	v_max_f32_e32 v219, 0x3985b185, v219
	v_rcp_f32_e32 v212, v212
	v_rcp_f32_e32 v213, v213
	v_rcp_f32_e32 v214, v214
	v_rcp_f32_e32 v215, v215
	v_rcp_f32_e32 v216, v216
	v_rcp_f32_e32 v217, v217
	v_rcp_f32_e32 v218, v218
	v_rcp_f32_e32 v219, v219
	v_cvt_f32_ubyte0_e32 v204, v40
	v_cvt_f32_ubyte1_e32 v205, v40
	v_cvt_f32_ubyte2_e32 v206, v40
	v_cvt_f32_ubyte3_e32 v207, v40
	v_cvt_f32_ubyte0_e32 v208, v41
	v_cvt_f32_ubyte1_e32 v209, v41
	v_cvt_f32_ubyte2_e32 v210, v41
	v_cvt_f32_ubyte3_e32 v211, v41
	v_pk_mul_f32 v[212:213], v[212:213], v[204:205]
	v_pk_mul_f32 v[214:215], v[214:215], v[206:207]
	v_pk_mul_f32 v[216:217], v[216:217], v[208:209]
	v_pk_mul_f32 v[218:219], v[218:219], v[210:211]
	v_pk_mul_f32 v[128:129], v[128:129], v[212:213]
	v_pk_mul_f32 v[130:131], v[130:131], v[214:215]
	v_pk_mul_f32 v[124:125], v[124:125], v[216:217]
	v_pk_mul_f32 v[126:127], v[126:127], v[218:219]
	s_waitcnt vmcnt(16)
; __device__ __forceinline__ u32x4 pack8(const f32x4 a, const f32x4 b) { u32x4 w; w.x = cvt_pk_bf16(a[0], a[1]); w.y = cvt_pk_bf16(a[2], a[3]); w.z = cvt_pk_bf16(b[0], b[1]); w.w = cvt_pk_bf16(b[2], b[3]); return w; }
;     __device__ __forceinline__ void operator()(f32x4 (&acc)[2][2][4][2], const Unit& u, int wr, int wc, int fr, int fq) const {
;     ...
;                 for (int bj = 0; bj < 2; ++bj) { const u32x2 a2 = ga[c & 1][m2][bj], b2 = gb[c & 1][m2][bj]; const float q = 1.0f / 255.0f;
;                     const f32x4 sa0 = {(float)((a2.x >> 0) & 0xffu), (float)((a2.x >> 8) & 0xffu), (float)((a2.x >> 16) & 0xffu), (float)((a2.x >> 24) & 0xffu)};
;                     const f32x4 sa1 = {(float)((a2.y >> 0) & 0xffu), (float)((a2.y >> 8) & 0xffu), (float)((a2.y >> 16) & 0xffu), (float)((a2.y >> 24) & 0xffu)};
;                     f32x4 sb0 = {(float)((b2.x >> 0) & 0xffu), (float)((b2.x >> 8) & 0xffu), (float)((b2.x >> 16) & 0xffu), (float)((b2.x >> 24) & 0xffu)};
;                     f32x4 sb1 = {(float)((b2.y >> 0) & 0xffu), (float)((b2.y >> 8) & 0xffu), (float)((b2.y >> 16) & 0xffu), (float)((b2.y >> 24) & 0xffu)};
; #pragma unroll
;                     for (int e = 0; e < 4; ++e) { sb0[e] = fmaxf(sb0[e], 2.55e-4f); sb1[e] = fmaxf(sb1[e], 2.55e-4f); }
;                     if (second) *(u32x4*)(MERGED + (size_t)(row0 + ai * HALF + m * 16) * DM + col0 + bj * HALF) = pack8(acc[ai][bj][m][0] * (sb0 * q), acc[ai][bj][m][1] * (sb1 * q));
;                     if (!second) { f32x4 r0, r1;
; #pragma unroll
;                         for (int e = 0; e < 4; ++e) { r0[e] = sa0[e] * __builtin_amdgcn_rcpf(sb0[e]); r1[e] = sa1[e] * __builtin_amdgcn_rcpf(sb1[e]); }
;                         acc[ai][bj][m][0] = acc[ai][bj][m][0] * r0; acc[ai][bj][m][1] = acc[ai][bj][m][1] * r1; }
	v_cvt_f32_ubyte0_e32 v212, v38
	v_cvt_f32_ubyte1_e32 v213, v38
	v_cvt_f32_ubyte2_e32 v214, v38
	v_cvt_f32_ubyte3_e32 v215, v38
	v_cvt_f32_ubyte0_e32 v216, v39
	v_cvt_f32_ubyte1_e32 v217, v39
	v_cvt_f32_ubyte2_e32 v218, v39
	v_cvt_f32_ubyte3_e32 v219, v39
	v_max_f32_e32 v212, 0x3985b185, v212
	v_max_f32_e32 v213, 0x3985b185, v213
	v_max_f32_e32 v214, 0x3985b185, v214
	v_max_f32_e32 v215, 0x3985b185, v215
	v_max_f32_e32 v216, 0x3985b185, v216
	v_max_f32_e32 v217, 0x3985b185, v217
	v_max_f32_e32 v218, 0x3985b185, v218
	v_max_f32_e32 v219, 0x3985b185, v219
	v_rcp_f32_e32 v212, v212
	v_rcp_f32_e32 v213, v213
	v_rcp_f32_e32 v214, v214
	v_rcp_f32_e32 v215, v215
	v_rcp_f32_e32 v216, v216
	v_rcp_f32_e32 v217, v217
	v_rcp_f32_e32 v218, v218
	v_rcp_f32_e32 v219, v219
	v_cvt_f32_ubyte0_e32 v204, v42
	v_cvt_f32_ubyte1_e32 v205, v42
	v_cvt_f32_ubyte2_e32 v206, v42
	v_cvt_f32_ubyte3_e32 v207, v42
	v_cvt_f32_ubyte0_e32 v208, v43
	v_cvt_f32_ubyte1_e32 v209, v43
	v_cvt_f32_ubyte2_e32 v210, v43
	v_cvt_f32_ubyte3_e32 v211, v43
	v_pk_mul_f32 v[212:213], v[212:213], v[204:205]
	v_pk_mul_f32 v[214:215], v[214:215], v[206:207]
	v_pk_mul_f32 v[216:217], v[216:217], v[208:209]
	v_pk_mul_f32 v[218:219], v[218:219], v[210:211]
	v_pk_mul_f32 v[112:113], v[112:113], v[212:213]
	v_pk_mul_f32 v[114:115], v[114:115], v[214:215]
	v_pk_mul_f32 v[108:109], v[108:109], v[216:217]
	v_pk_mul_f32 v[110:111], v[110:111], v[218:219]
	s_waitcnt vmcnt(14)
	v_cvt_f32_ubyte0_e32 v212, v68
	v_cvt_f32_ubyte1_e32 v213, v68
	v_cvt_f32_ubyte2_e32 v214, v68
	v_cvt_f32_ubyte3_e32 v215, v68
	v_cvt_f32_ubyte0_e32 v216, v69
	v_cvt_f32_ubyte1_e32 v217, v69
	v_cvt_f32_ubyte2_e32 v218, v69
	v_cvt_f32_ubyte3_e32 v219, v69
	v_max_f32_e32 v212, 0x3985b185, v212
	v_max_f32_e32 v213, 0x3985b185, v213
	v_max_f32_e32 v214, 0x3985b185, v214
	v_max_f32_e32 v215, 0x3985b185, v215
	v_max_f32_e32 v216, 0x3985b185, v216
	v_max_f32_e32 v217, 0x3985b185, v217
	v_max_f32_e32 v218, 0x3985b185, v218
	v_max_f32_e32 v219, 0x3985b185, v219
	v_rcp_f32_e32 v212, v212
	v_rcp_f32_e32 v213, v213
	v_rcp_f32_e32 v214, v214
	v_rcp_f32_e32 v215, v215
	v_rcp_f32_e32 v216, v216
	v_rcp_f32_e32 v217, v217
	v_rcp_f32_e32 v218, v218
	v_rcp_f32_e32 v219, v219
	v_cvt_f32_ubyte0_e32 v204, v72
	v_cvt_f32_ubyte1_e32 v205, v72
	v_cvt_f32_ubyte2_e32 v206, v72
	v_cvt_f32_ubyte3_e32 v207, v72
	v_cvt_f32_ubyte0_e32 v208, v73
	v_cvt_f32_ubyte1_e32 v209, v73
	v_cvt_f32_ubyte2_e32 v210, v73
	v_cvt_f32_ubyte3_e32 v211, v73
	v_pk_mul_f32 v[212:213], v[212:213], v[204:205]
	v_pk_mul_f32 v[214:215], v[214:215], v[206:207]
	v_pk_mul_f32 v[216:217], v[216:217], v[208:209]
	v_pk_mul_f32 v[218:219], v[218:219], v[210:211]
	v_pk_mul_f32 v[96:97], v[96:97], v[212:213]
	v_pk_mul_f32 v[98:99], v[98:99], v[214:215]
	v_pk_mul_f32 v[92:93], v[92:93], v[216:217]
	v_pk_mul_f32 v[94:95], v[94:95], v[218:219]
	s_waitcnt vmcnt(12)
	v_cvt_f32_ubyte0_e32 v212, v70
	v_cvt_f32_ubyte1_e32 v213, v70
	v_cvt_f32_ubyte2_e32 v214, v70
	v_cvt_f32_ubyte3_e32 v215, v70
	v_cvt_f32_ubyte0_e32 v216, v71
	v_cvt_f32_ubyte1_e32 v217, v71
	v_cvt_f32_ubyte2_e32 v218, v71
	v_cvt_f32_ubyte3_e32 v219, v71
	v_max_f32_e32 v212, 0x3985b185, v212
	v_max_f32_e32 v213, 0x3985b185, v213
	v_max_f32_e32 v214, 0x3985b185, v214
	v_max_f32_e32 v215, 0x3985b185, v215
	v_max_f32_e32 v216, 0x3985b185, v216
	v_max_f32_e32 v217, 0x3985b185, v217
	v_max_f32_e32 v218, 0x3985b185, v218
	v_max_f32_e32 v219, 0x3985b185, v219
	v_rcp_f32_e32 v212, v212
	v_rcp_f32_e32 v213, v213
	v_rcp_f32_e32 v214, v214
	v_rcp_f32_e32 v215, v215
	v_rcp_f32_e32 v216, v216
	v_rcp_f32_e32 v217, v217
	v_rcp_f32_e32 v218, v218
	v_rcp_f32_e32 v219, v219
	v_cvt_f32_ubyte0_e32 v204, v74
	v_cvt_f32_ubyte1_e32 v205, v74
	v_cvt_f32_ubyte2_e32 v206, v74
	v_cvt_f32_ubyte3_e32 v207, v74
	v_cvt_f32_ubyte0_e32 v208, v75
	v_cvt_f32_ubyte1_e32 v209, v75
	v_cvt_f32_ubyte2_e32 v210, v75
	v_cvt_f32_ubyte3_e32 v211, v75
	v_pk_mul_f32 v[212:213], v[212:213], v[204:205]
	v_pk_mul_f32 v[214:215], v[214:215], v[206:207]
	v_pk_mul_f32 v[216:217], v[216:217], v[208:209]
	v_pk_mul_f32 v[218:219], v[218:219], v[210:211]
	v_pk_mul_f32 v[80:81], v[80:81], v[212:213]
	v_pk_mul_f32 v[82:83], v[82:83], v[214:215]
	v_pk_mul_f32 v[76:77], v[76:77], v[216:217]
	v_pk_mul_f32 v[78:79], v[78:79], v[218:219]
	s_waitcnt vmcnt(10)
	v_cvt_f32_ubyte0_e32 v212, v100
	v_cvt_f32_ubyte1_e32 v213, v100
	v_cvt_f32_ubyte2_e32 v214, v100
	v_cvt_f32_ubyte3_e32 v215, v100
	v_cvt_f32_ubyte0_e32 v216, v101
	v_cvt_f32_ubyte1_e32 v217, v101
	v_cvt_f32_ubyte2_e32 v218, v101
	v_cvt_f32_ubyte3_e32 v219, v101
	v_max_f32_e32 v212, 0x3985b185, v212
	v_max_f32_e32 v213, 0x3985b185, v213
	v_max_f32_e32 v214, 0x3985b185, v214
	v_max_f32_e32 v215, 0x3985b185, v215
	v_max_f32_e32 v216, 0x3985b185, v216
	v_max_f32_e32 v217, 0x3985b185, v217
	v_max_f32_e32 v218, 0x3985b185, v218
	v_max_f32_e32 v219, 0x3985b185, v219
	v_rcp_f32_e32 v212, v212
	v_rcp_f32_e32 v213, v213
	v_rcp_f32_e32 v214, v214
	v_rcp_f32_e32 v215, v215
	v_rcp_f32_e32 v216, v216
	v_rcp_f32_e32 v217, v217
	v_rcp_f32_e32 v218, v218
	v_rcp_f32_e32 v219, v219
	v_cvt_f32_ubyte0_e32 v204, v104
	v_cvt_f32_ubyte1_e32 v205, v104
	v_cvt_f32_ubyte2_e32 v206, v104
	v_cvt_f32_ubyte3_e32 v207, v104
	v_cvt_f32_ubyte0_e32 v208, v105
	v_cvt_f32_ubyte1_e32 v209, v105
	v_cvt_f32_ubyte2_e32 v210, v105
	v_cvt_f32_ubyte3_e32 v211, v105
	v_pk_mul_f32 v[212:213], v[212:213], v[204:205]
	v_pk_mul_f32 v[214:215], v[214:215], v[206:207]
	v_pk_mul_f32 v[216:217], v[216:217], v[208:209]
	v_pk_mul_f32 v[218:219], v[218:219], v[210:211]
	v_pk_mul_f32 v[64:65], v[64:65], v[212:213]
	v_pk_mul_f32 v[66:67], v[66:67], v[214:215]
	v_pk_mul_f32 v[60:61], v[60:61], v[216:217]
	v_pk_mul_f32 v[62:63], v[62:63], v[218:219]
	s_waitcnt vmcnt(8)
; __device__ __forceinline__ u32x4 pack8(const f32x4 a, const f32x4 b) { u32x4 w; w.x = cvt_pk_bf16(a[0], a[1]); w.y = cvt_pk_bf16(a[2], a[3]); w.z = cvt_pk_bf16(b[0], b[1]); w.w = cvt_pk_bf16(b[2], b[3]); return w; }
;     __device__ __forceinline__ void operator()(f32x4 (&acc)[2][2][4][2], const Unit& u, int wr, int wc, int fr, int fq) const {
;     ...
;                 for (int bj = 0; bj < 2; ++bj) { const u32x2 a2 = ga[c & 1][m2][bj], b2 = gb[c & 1][m2][bj]; const float q = 1.0f / 255.0f;
;                     const f32x4 sa0 = {(float)((a2.x >> 0) & 0xffu), (float)((a2.x >> 8) & 0xffu), (float)((a2.x >> 16) & 0xffu), (float)((a2.x >> 24) & 0xffu)};
;                     const f32x4 sa1 = {(float)((a2.y >> 0) & 0xffu), (float)((a2.y >> 8) & 0xffu), (float)((a2.y >> 16) & 0xffu), (float)((a2.y >> 24) & 0xffu)};
;                     f32x4 sb0 = {(float)((b2.x >> 0) & 0xffu), (float)((b2.x >> 8) & 0xffu), (float)((b2.x >> 16) & 0xffu), (float)((b2.x >> 24) & 0xffu)};
;                     f32x4 sb1 = {(float)((b2.y >> 0) & 0xffu), (float)((b2.y >> 8) & 0xffu), (float)((b2.y >> 16) & 0xffu), (float)((b2.y >> 24) & 0xffu)};
; #pragma unroll
;                     for (int e = 0; e < 4; ++e) { sb0[e] = fmaxf(sb0[e], 2.55e-4f); sb1[e] = fmaxf(sb1[e], 2.55e-4f); }
;                     if (second) *(u32x4*)(MERGED + (size_t)(row0 + ai * HALF + m * 16) * DM + col0 + bj * HALF) = pack8(acc[ai][bj][m][0] * (sb0 * q), acc[ai][bj][m][1] * (sb1 * q));
;                     if (!second) { f32x4 r0, r1;
; #pragma unroll
;                         for (int e = 0; e < 4; ++e) { r0[e] = sa0[e] * __builtin_amdgcn_rcpf(sb0[e]); r1[e] = sa1[e] * __builtin_amdgcn_rcpf(sb1[e]); }
;                         acc[ai][bj][m][0] = acc[ai][bj][m][0] * r0; acc[ai][bj][m][1] = acc[ai][bj][m][1] * r1; }
	v_cvt_f32_ubyte0_e32 v212, v102
	v_cvt_f32_ubyte1_e32 v213, v102
	v_cvt_f32_ubyte2_e32 v214, v102
	v_cvt_f32_ubyte3_e32 v215, v102
	v_cvt_f32_ubyte0_e32 v216, v103
	v_cvt_f32_ubyte1_e32 v217, v103
	v_cvt_f32_ubyte2_e32 v218, v103
	v_cvt_f32_ubyte3_e32 v219, v103
	v_max_f32_e32 v212, 0x3985b185, v212
	v_max_f32_e32 v213, 0x3985b185, v213
	v_max_f32_e32 v214, 0x3985b185, v214
	v_max_f32_e32 v215, 0x3985b185, v215
	v_max_f32_e32 v216, 0x3985b185, v216
	v_max_f32_e32 v217, 0x3985b185, v217
	v_max_f32_e32 v218, 0x3985b185, v218
	v_max_f32_e32 v219, 0x3985b185, v219
	v_rcp_f32_e32 v212, v212
	v_rcp_f32_e32 v213, v213
	v_rcp_f32_e32 v214, v214
	v_rcp_f32_e32 v215, v215
	v_rcp_f32_e32 v216, v216
	v_rcp_f32_e32 v217, v217
	v_rcp_f32_e32 v218, v218
	v_rcp_f32_e32 v219, v219
	v_cvt_f32_ubyte0_e32 v204, v106
	v_cvt_f32_ubyte1_e32 v205, v106
	v_cvt_f32_ubyte2_e32 v206, v106
	v_cvt_f32_ubyte3_e32 v207, v106
	v_cvt_f32_ubyte0_e32 v208, v107
	v_cvt_f32_ubyte1_e32 v209, v107
	v_cvt_f32_ubyte2_e32 v210, v107
	v_cvt_f32_ubyte3_e32 v211, v107
	v_pk_mul_f32 v[212:213], v[212:213], v[204:205]
	v_pk_mul_f32 v[214:215], v[214:215], v[206:207]
	v_pk_mul_f32 v[216:217], v[216:217], v[208:209]
	v_pk_mul_f32 v[218:219], v[218:219], v[210:211]
	v_pk_mul_f32 v[48:49], v[48:49], v[212:213]
	v_pk_mul_f32 v[50:51], v[50:51], v[214:215]
	v_pk_mul_f32 v[44:45], v[44:45], v[216:217]
	v_pk_mul_f32 v[46:47], v[46:47], v[218:219]
	s_waitcnt vmcnt(6)
	v_cvt_f32_ubyte0_e32 v212, v132
	v_cvt_f32_ubyte1_e32 v213, v132
	v_cvt_f32_ubyte2_e32 v214, v132
	v_cvt_f32_ubyte3_e32 v215, v132
	v_cvt_f32_ubyte0_e32 v216, v133
	v_cvt_f32_ubyte1_e32 v217, v133
	v_cvt_f32_ubyte2_e32 v218, v133
	v_cvt_f32_ubyte3_e32 v219, v133
	v_max_f32_e32 v212, 0x3985b185, v212
	v_max_f32_e32 v213, 0x3985b185, v213
	v_max_f32_e32 v214, 0x3985b185, v214
	v_max_f32_e32 v215, 0x3985b185, v215
	v_max_f32_e32 v216, 0x3985b185, v216
	v_max_f32_e32 v217, 0x3985b185, v217
	v_max_f32_e32 v218, 0x3985b185, v218
	v_max_f32_e32 v219, 0x3985b185, v219
	v_rcp_f32_e32 v212, v212
	v_rcp_f32_e32 v213, v213
	v_rcp_f32_e32 v214, v214
	v_rcp_f32_e32 v215, v215
	v_rcp_f32_e32 v216, v216
	v_rcp_f32_e32 v217, v217
	v_rcp_f32_e32 v218, v218
	v_rcp_f32_e32 v219, v219
	v_cvt_f32_ubyte0_e32 v204, v136
	v_cvt_f32_ubyte1_e32 v205, v136
	v_cvt_f32_ubyte2_e32 v206, v136
	v_cvt_f32_ubyte3_e32 v207, v136
	v_cvt_f32_ubyte0_e32 v208, v137
	v_cvt_f32_ubyte1_e32 v209, v137
	v_cvt_f32_ubyte2_e32 v210, v137
	v_cvt_f32_ubyte3_e32 v211, v137
	v_pk_mul_f32 v[212:213], v[212:213], v[204:205]
	v_pk_mul_f32 v[214:215], v[214:215], v[206:207]
	v_pk_mul_f32 v[216:217], v[216:217], v[208:209]
	v_pk_mul_f32 v[218:219], v[218:219], v[210:211]
	v_pk_mul_f32 v[32:33], v[32:33], v[212:213]
	v_pk_mul_f32 v[34:35], v[34:35], v[214:215]
	v_pk_mul_f32 v[28:29], v[28:29], v[216:217]
	v_pk_mul_f32 v[30:31], v[30:31], v[218:219]
	s_waitcnt vmcnt(4)
	v_cvt_f32_ubyte0_e32 v212, v134
	v_cvt_f32_ubyte1_e32 v213, v134
	v_cvt_f32_ubyte2_e32 v214, v134
	v_cvt_f32_ubyte3_e32 v215, v134
	v_cvt_f32_ubyte0_e32 v216, v135
	v_cvt_f32_ubyte1_e32 v217, v135
	v_cvt_f32_ubyte2_e32 v218, v135
	v_cvt_f32_ubyte3_e32 v219, v135
	v_max_f32_e32 v212, 0x3985b185, v212
	v_max_f32_e32 v213, 0x3985b185, v213
	v_max_f32_e32 v214, 0x3985b185, v214
	v_max_f32_e32 v215, 0x3985b185, v215
	v_max_f32_e32 v216, 0x3985b185, v216
	v_max_f32_e32 v217, 0x3985b185, v217
	v_max_f32_e32 v218, 0x3985b185, v218
	v_max_f32_e32 v219, 0x3985b185, v219
	v_rcp_f32_e32 v212, v212
	v_rcp_f32_e32 v213, v213
	v_rcp_f32_e32 v214, v214
	v_rcp_f32_e32 v215, v215
	v_rcp_f32_e32 v216, v216
	v_rcp_f32_e32 v217, v217
	v_rcp_f32_e32 v218, v218
	v_rcp_f32_e32 v219, v219
	v_cvt_f32_ubyte0_e32 v204, v138
	v_cvt_f32_ubyte1_e32 v205, v138
	v_cvt_f32_ubyte2_e32 v206, v138
	v_cvt_f32_ubyte3_e32 v207, v138
	v_cvt_f32_ubyte0_e32 v208, v139
	v_cvt_f32_ubyte1_e32 v209, v139
	v_cvt_f32_ubyte2_e32 v210, v139
	v_cvt_f32_ubyte3_e32 v211, v139
	v_pk_mul_f32 v[212:213], v[212:213], v[204:205]
	v_pk_mul_f32 v[214:215], v[214:215], v[206:207]
	v_pk_mul_f32 v[216:217], v[216:217], v[208:209]
	v_pk_mul_f32 v[218:219], v[218:219], v[210:211]
	v_pk_mul_f32 v[24:25], v[24:25], v[212:213]
	v_pk_mul_f32 v[26:27], v[26:27], v[214:215]
	v_pk_mul_f32 v[20:21], v[20:21], v[216:217]
	v_pk_mul_f32 v[22:23], v[22:23], v[218:219]
	s_waitcnt vmcnt(2)
	v_cvt_f32_ubyte0_e32 v212, v174
	v_cvt_f32_ubyte1_e32 v213, v174
	v_cvt_f32_ubyte2_e32 v214, v174
	v_cvt_f32_ubyte3_e32 v215, v174
	v_cvt_f32_ubyte0_e32 v216, v175
	v_cvt_f32_ubyte1_e32 v217, v175
	v_cvt_f32_ubyte2_e32 v218, v175
	v_cvt_f32_ubyte3_e32 v219, v175
	v_max_f32_e32 v212, 0x3985b185, v212
	v_max_f32_e32 v213, 0x3985b185, v213
	v_max_f32_e32 v214, 0x3985b185, v214
	v_max_f32_e32 v215, 0x3985b185, v215
	v_max_f32_e32 v216, 0x3985b185, v216
	v_max_f32_e32 v217, 0x3985b185, v217
	v_max_f32_e32 v218, 0x3985b185, v218
	v_max_f32_e32 v219, 0x3985b185, v219
	v_rcp_f32_e32 v212, v212
	v_rcp_f32_e32 v213, v213
	v_rcp_f32_e32 v214, v214
	v_rcp_f32_e32 v215, v215
	v_rcp_f32_e32 v216, v216
	v_rcp_f32_e32 v217, v217
	v_rcp_f32_e32 v218, v218
	v_rcp_f32_e32 v219, v219
	v_cvt_f32_ubyte0_e32 v204, v178
	v_cvt_f32_ubyte1_e32 v205, v178
	v_cvt_f32_ubyte2_e32 v206, v178
	v_cvt_f32_ubyte3_e32 v207, v178
	v_cvt_f32_ubyte0_e32 v208, v179
	v_cvt_f32_ubyte1_e32 v209, v179
	v_cvt_f32_ubyte2_e32 v210, v179
	v_cvt_f32_ubyte3_e32 v211, v179
	v_pk_mul_f32 v[212:213], v[212:213], v[204:205]
	v_pk_mul_f32 v[214:215], v[214:215], v[206:207]
	v_pk_mul_f32 v[216:217], v[216:217], v[208:209]
	v_pk_mul_f32 v[218:219], v[218:219], v[210:211]
	v_pk_mul_f32 v[16:17], v[16:17], v[212:213]
	v_pk_mul_f32 v[18:19], v[18:19], v[214:215]
	v_pk_mul_f32 v[12:13], v[12:13], v[216:217]
	v_pk_mul_f32 v[14:15], v[14:15], v[218:219]
	s_waitcnt vmcnt(0)
; __device__ __forceinline__ u32x4 pack8(const f32x4 a, const f32x4 b) { u32x4 w; w.x = cvt_pk_bf16(a[0], a[1]); w.y = cvt_pk_bf16(a[2], a[3]); w.z = cvt_pk_bf16(b[0], b[1]); w.w = cvt_pk_bf16(b[2], b[3]); return w; }
;     __device__ __forceinline__ void operator()(f32x4 (&acc)[2][2][4][2], const Unit& u, int wr, int wc, int fr, int fq) const {
;     ...
;         MG_LOAD(0, 0); MG_LOAD(1, 1);
;         asm volatile("" ::: "memory");
; #pragma unroll
;         for (int c = 0; c < 4; ++c) { const int ai = c >> 1;
; #pragma unroll
;             for (int m2 = 0; m2 < 2; ++m2) { const int m = 2 * (c & 1) + m2;
; #pragma unroll
;                 for (int bj = 0; bj < 2; ++bj) { const u32x2 a2 = ga[c & 1][m2][bj], b2 = gb[c & 1][m2][bj]; const float q = 1.0f / 255.0f;
;                     const f32x4 sa0 = {(float)((a2.x >> 0) & 0xffu), (float)((a2.x >> 8) & 0xffu), (float)((a2.x >> 16) & 0xffu), (float)((a2.x >> 24) & 0xffu)};
;                     const f32x4 sa1 = {(float)((a2.y >> 0) & 0xffu), (float)((a2.y >> 8) & 0xffu), (float)((a2.y >> 16) & 0xffu), (float)((a2.y >> 24) & 0xffu)};
;                     f32x4 sb0 = {(float)((b2.x >> 0) & 0xffu), (float)((b2.x >> 8) & 0xffu), (float)((b2.x >> 16) & 0xffu), (float)((b2.x >> 24) & 0xffu)};
;                     f32x4 sb1 = {(float)((b2.y >> 0) & 0xffu), (float)((b2.y >> 8) & 0xffu), (float)((b2.y >> 16) & 0xffu), (float)((b2.y >> 24) & 0xffu)};
; #pragma unroll
;                     for (int e = 0; e < 4; ++e) { sb0[e] = fmaxf(sb0[e], 2.55e-4f); sb1[e] = fmaxf(sb1[e], 2.55e-4f); }
;                     if (second) *(u32x4*)(MERGED + (size_t)(row0 + ai * HALF + m * 16) * DM + col0 + bj * HALF) = pack8(acc[ai][bj][m][0] * (sb0 * q), acc[ai][bj][m][1] * (sb1 * q));
;                     if (!second) { f32x4 r0, r1;
; #pragma unroll
;                         for (int e = 0; e < 4; ++e) { r0[e] = sa0[e] * __builtin_amdgcn_rcpf(sb0[e]); r1[e] = sa1[e] * __builtin_amdgcn_rcpf(sb1[e]); }
;                         acc[ai][bj][m][0] = acc[ai][bj][m][0] * r0; acc[ai][bj][m][1] = acc[ai][bj][m][1] * r1; }
;                     else { acc[ai][bj][m][0] = (f32x4){0.f, 0.f, 0.f, 0.f}; acc[ai][bj][m][1] = (f32x4){0.f, 0.f, 0.f, 0.f}; } }
	v_cvt_f32_ubyte0_e32 v212, v176
	v_cvt_f32_ubyte1_e32 v213, v176
	v_cvt_f32_ubyte2_e32 v214, v176
	v_cvt_f32_ubyte3_e32 v215, v176
	v_cvt_f32_ubyte0_e32 v216, v177
	v_cvt_f32_ubyte1_e32 v217, v177
	v_cvt_f32_ubyte2_e32 v218, v177
	v_cvt_f32_ubyte3_e32 v219, v177
	v_max_f32_e32 v212, 0x3985b185, v212
	v_max_f32_e32 v213, 0x3985b185, v213
	v_max_f32_e32 v214, 0x3985b185, v214
	v_max_f32_e32 v215, 0x3985b185, v215
	v_max_f32_e32 v216, 0x3985b185, v216
	v_max_f32_e32 v217, 0x3985b185, v217
	v_max_f32_e32 v218, 0x3985b185, v218
	v_max_f32_e32 v219, 0x3985b185, v219
	v_rcp_f32_e32 v212, v212
	v_rcp_f32_e32 v213, v213
	v_rcp_f32_e32 v214, v214
	v_rcp_f32_e32 v215, v215
	v_rcp_f32_e32 v216, v216
	v_rcp_f32_e32 v217, v217
	v_rcp_f32_e32 v218, v218
	v_rcp_f32_e32 v219, v219
	v_cvt_f32_ubyte0_e32 v204, v180
	v_cvt_f32_ubyte1_e32 v205, v180
	v_cvt_f32_ubyte2_e32 v206, v180
	v_cvt_f32_ubyte3_e32 v207, v180
	v_cvt_f32_ubyte0_e32 v208, v181
	v_cvt_f32_ubyte1_e32 v209, v181
	v_cvt_f32_ubyte2_e32 v210, v181
	v_cvt_f32_ubyte3_e32 v211, v181
	v_pk_mul_f32 v[212:213], v[212:213], v[204:205]
	v_pk_mul_f32 v[214:215], v[214:215], v[206:207]
	v_pk_mul_f32 v[216:217], v[216:217], v[208:209]
	v_pk_mul_f32 v[218:219], v[218:219], v[210:211]
	v_pk_mul_f32 v[8:9], v[8:9], v[212:213]
	v_pk_mul_f32 v[10:11], v[10:11], v[214:215]
	v_pk_mul_f32 v[4:5], v[4:5], v[216:217]
	v_pk_mul_f32 v[6:7], v[6:7], v[218:219]
	s_branch .Lmg_end
.Lmg_second:
	v_add_u32_e32 v252, 0x4000, v252
	global_load_dwordx2 v[36:37], v252, s[10:11]
	global_load_dwordx2 v[38:39], v252, s[10:11] offset:128
	v_add_u32_e32 v252, 0x4000, v252
	global_load_dwordx2 v[40:41], v252, s[10:11]
	global_load_dwordx2 v[42:43], v252, s[10:11] offset:128
	s_waitcnt vmcnt(15)
	v_cvt_f32_ubyte0_e32 v212, v228
	v_cvt_f32_ubyte1_e32 v213, v228
	v_cvt_f32_ubyte2_e32 v214, v228
	v_cvt_f32_ubyte3_e32 v215, v228
	v_cvt_f32_ubyte0_e32 v216, v229
	v_cvt_f32_ubyte1_e32 v217, v229
	v_cvt_f32_ubyte2_e32 v218, v229
	v_cvt_f32_ubyte3_e32 v219, v229
	v_max_f32_e32 v212, 0x3985b185, v212
	v_max_f32_e32 v213, 0x3985b185, v213
	v_max_f32_e32 v214, 0x3985b185, v214
	v_max_f32_e32 v215, 0x3985b185, v215
	v_max_f32_e32 v216, 0x3985b185, v216
	v_max_f32_e32 v217, 0x3985b185, v217
	v_max_f32_e32 v218, 0x3985b185, v218
	v_max_f32_e32 v219, 0x3985b185, v219
	v_pk_mul_f32 v[212:213], v[212:213], s[54:55] op_sel_hi:[1,0]
	v_pk_mul_f32 v[214:215], v[214:215], s[54:55] op_sel_hi:[1,0]
	v_pk_mul_f32 v[216:217], v[216:217], s[54:55] op_sel_hi:[1,0]
	v_pk_mul_f32 v[218:219], v[218:219], s[54:55] op_sel_hi:[1,0]
	v_pk_mul_f32 v[212:213], v[56:57], v[212:213]
	v_pk_mul_f32 v[214:215], v[58:59], v[214:215]
	v_pk_mul_f32 v[216:217], v[52:53], v[216:217]
	v_pk_mul_f32 v[218:219], v[54:55], v[218:219]
	v_cvt_pk_bf16_f32 v192, v212, v213
	v_cvt_pk_bf16_f32 v193, v214, v215
	v_cvt_pk_bf16_f32 v194, v216, v217
	v_cvt_pk_bf16_f32 v195, v218, v219
	global_store_dwordx4 v253, v[192:195], s[12:13]
	s_waitcnt vmcnt(15)
	v_cvt_f32_ubyte0_e32 v212, v230
	v_cvt_f32_ubyte1_e32 v213, v230
	v_cvt_f32_ubyte2_e32 v214, v230
	v_cvt_f32_ubyte3_e32 v215, v230
	v_cvt_f32_ubyte0_e32 v216, v231
	v_cvt_f32_ubyte1_e32 v217, v231
	v_cvt_f32_ubyte2_e32 v218, v231
	v_cvt_f32_ubyte3_e32 v219, v231
	v_max_f32_e32 v212, 0x3985b185, v212
	v_max_f32_e32 v213, 0x3985b185, v213
	v_max_f32_e32 v214, 0x3985b185, v214
	v_max_f32_e32 v215, 0x3985b185, v215
	v_max_f32_e32 v216, 0x3985b185, v216
	v_max_f32_e32 v217, 0x3985b185, v217
	v_max_f32_e32 v218, 0x3985b185, v218
	v_max_f32_e32 v219, 0x3985b185, v219
	v_pk_mul_f32 v[212:213], v[212:213], s[54:55] op_sel_hi:[1,0]
	v_pk_mul_f32 v[214:215], v[214:215], s[54:55] op_sel_hi:[1,0]
	v_pk_mul_f32 v[216:217], v[216:217], s[54:55] op_sel_hi:[1,0]
	v_pk_mul_f32 v[218:219], v[218:219], s[54:55] op_sel_hi:[1,0]
	v_pk_mul_f32 v[212:213], v[160:161], v[212:213]
	v_pk_mul_f32 v[214:215], v[162:163], v[214:215]
	v_pk_mul_f32 v[216:217], v[156:157], v[216:217]
	v_pk_mul_f32 v[218:219], v[158:159], v[218:219]
	v_cvt_pk_bf16_f32 v196, v212, v213
	v_cvt_pk_bf16_f32 v197, v214, v215
	v_cvt_pk_bf16_f32 v198, v216, v217
	v_cvt_pk_bf16_f32 v199, v218, v219
	global_store_dwordx4 v253, v[196:199], s[12:13] offset:256
	v_add_u32_e32 v253, 0x8000, v253
	s_waitcnt vmcnt(15)
	v_cvt_f32_ubyte0_e32 v212, v232
	v_cvt_f32_ubyte1_e32 v213, v232
	v_cvt_f32_ubyte2_e32 v214, v232
	v_cvt_f32_ubyte3_e32 v215, v232
	v_cvt_f32_ubyte0_e32 v216, v233
	v_cvt_f32_ubyte1_e32 v217, v233
	v_cvt_f32_ubyte2_e32 v218, v233
	v_cvt_f32_ubyte3_e32 v219, v233
	v_max_f32_e32 v212, 0x3985b185, v212
	v_max_f32_e32 v213, 0x3985b185, v213
	v_max_f32_e32 v214, 0x3985b185, v214
	v_max_f32_e32 v215, 0x3985b185, v215
	v_max_f32_e32 v216, 0x3985b185, v216
	v_max_f32_e32 v217, 0x3985b185, v217
	v_max_f32_e32 v218, 0x3985b185, v218
	v_max_f32_e32 v219, 0x3985b185, v219
	v_pk_mul_f32 v[212:213], v[212:213], s[54:55] op_sel_hi:[1,0]
	v_pk_mul_f32 v[214:215], v[214:215], s[54:55] op_sel_hi:[1,0]
	v_pk_mul_f32 v[216:217], v[216:217], s[54:55] op_sel_hi:[1,0]
	v_pk_mul_f32 v[218:219], v[218:219], s[54:55] op_sel_hi:[1,0]
	v_pk_mul_f32 v[212:213], v[88:89], v[212:213]
	v_pk_mul_f32 v[214:215], v[90:91], v[214:215]
	v_pk_mul_f32 v[216:217], v[84:85], v[216:217]
	v_pk_mul_f32 v[218:219], v[86:87], v[218:219]
	v_cvt_pk_bf16_f32 v192, v212, v213
	v_cvt_pk_bf16_f32 v193, v214, v215
	v_cvt_pk_bf16_f32 v194, v216, v217
	v_cvt_pk_bf16_f32 v195, v218, v219
	global_store_dwordx4 v253, v[192:195], s[12:13]
	s_waitcnt vmcnt(15)
; __device__ __forceinline__ u32x4 pack8(const f32x4 a, const f32x4 b) { u32x4 w; w.x = cvt_pk_bf16(a[0], a[1]); w.y = cvt_pk_bf16(a[2], a[3]); w.z = cvt_pk_bf16(b[0], b[1]); w.w = cvt_pk_bf16(b[2], b[3]); return w; }
;     __device__ __forceinline__ void operator()(f32x4 (&acc)[2][2][4][2], const Unit& u, int wr, int wc, int fr, int fq) const {
;     ...
;                 for (int bj = 0; bj < 2; ++bj) { const u32x2 a2 = ga[c & 1][m2][bj], b2 = gb[c & 1][m2][bj]; const float q = 1.0f / 255.0f;
;                     const f32x4 sa0 = {(float)((a2.x >> 0) & 0xffu), (float)((a2.x >> 8) & 0xffu), (float)((a2.x >> 16) & 0xffu), (float)((a2.x >> 24) & 0xffu)};
;                     const f32x4 sa1 = {(float)((a2.y >> 0) & 0xffu), (float)((a2.y >> 8) & 0xffu), (float)((a2.y >> 16) & 0xffu), (float)((a2.y >> 24) & 0xffu)};
;                     f32x4 sb0 = {(float)((b2.x >> 0) & 0xffu), (float)((b2.x >> 8) & 0xffu), (float)((b2.x >> 16) & 0xffu), (float)((b2.x >> 24) & 0xffu)};
;                     f32x4 sb1 = {(float)((b2.y >> 0) & 0xffu), (float)((b2.y >> 8) & 0xffu), (float)((b2.y >> 16) & 0xffu), (float)((b2.y >> 24) & 0xffu)};
; #pragma unroll
;                     for (int e = 0; e < 4; ++e) { sb0[e] = fmaxf(sb0[e], 2.55e-4f); sb1[e] = fmaxf(sb1[e], 2.55e-4f); }
;                     if (second) *(u32x4*)(MERGED + (size_t)(row0 + ai * HALF + m * 16) * DM + col0 + bj * HALF) = pack8(acc[ai][bj][m][0] * (sb0 * q), acc[ai][bj][m][1] * (sb1 * q));
	v_cvt_f32_ubyte0_e32 v212, v234
	v_cvt_f32_ubyte1_e32 v213, v234
	v_cvt_f32_ubyte2_e32 v214, v234
	v_cvt_f32_ubyte3_e32 v215, v234
	v_cvt_f32_ubyte0_e32 v216, v235
	v_cvt_f32_ubyte1_e32 v217, v235
	v_cvt_f32_ubyte2_e32 v218, v235
	v_cvt_f32_ubyte3_e32 v219, v235
	v_max_f32_e32 v212, 0x3985b185, v212
	v_max_f32_e32 v213, 0x3985b185, v213
	v_max_f32_e32 v214, 0x3985b185, v214
	v_max_f32_e32 v215, 0x3985b185, v215
	v_max_f32_e32 v216, 0x3985b185, v216
	v_max_f32_e32 v217, 0x3985b185, v217
	v_max_f32_e32 v218, 0x3985b185, v218
	v_max_f32_e32 v219, 0x3985b185, v219
	v_pk_mul_f32 v[212:213], v[212:213], s[54:55] op_sel_hi:[1,0]
	v_pk_mul_f32 v[214:215], v[214:215], s[54:55] op_sel_hi:[1,0]
	v_pk_mul_f32 v[216:217], v[216:217], s[54:55] op_sel_hi:[1,0]
	v_pk_mul_f32 v[218:219], v[218:219], s[54:55] op_sel_hi:[1,0]
	v_pk_mul_f32 v[212:213], v[152:153], v[212:213]
	v_pk_mul_f32 v[214:215], v[154:155], v[214:215]
	v_pk_mul_f32 v[216:217], v[148:149], v[216:217]
	v_pk_mul_f32 v[218:219], v[150:151], v[218:219]
	v_cvt_pk_bf16_f32 v196, v212, v213
	v_cvt_pk_bf16_f32 v197, v214, v215
	v_cvt_pk_bf16_f32 v198, v216, v217
	v_cvt_pk_bf16_f32 v199, v218, v219
	global_store_dwordx4 v253, v[196:199], s[12:13] offset:256
	v_add_u32_e32 v253, 0x8000, v253
	s_waitcnt vmcnt(15)
	v_cvt_f32_ubyte0_e32 v212, v236
	v_cvt_f32_ubyte1_e32 v213, v236
	v_cvt_f32_ubyte2_e32 v214, v236
	v_cvt_f32_ubyte3_e32 v215, v236
	v_cvt_f32_ubyte0_e32 v216, v237
	v_cvt_f32_ubyte1_e32 v217, v237
	v_cvt_f32_ubyte2_e32 v218, v237
	v_cvt_f32_ubyte3_e32 v219, v237
	v_max_f32_e32 v212, 0x3985b185, v212
	v_max_f32_e32 v213, 0x3985b185, v213
	v_max_f32_e32 v214, 0x3985b185, v214
	v_max_f32_e32 v215, 0x3985b185, v215
	v_max_f32_e32 v216, 0x3985b185, v216
	v_max_f32_e32 v217, 0x3985b185, v217
	v_max_f32_e32 v218, 0x3985b185, v218
	v_max_f32_e32 v219, 0x3985b185, v219
	v_pk_mul_f32 v[212:213], v[212:213], s[54:55] op_sel_hi:[1,0]
	v_pk_mul_f32 v[214:215], v[214:215], s[54:55] op_sel_hi:[1,0]
	v_pk_mul_f32 v[216:217], v[216:217], s[54:55] op_sel_hi:[1,0]
	v_pk_mul_f32 v[218:219], v[218:219], s[54:55] op_sel_hi:[1,0]
	v_pk_mul_f32 v[212:213], v[120:121], v[212:213]
	v_pk_mul_f32 v[214:215], v[122:123], v[214:215]
	v_pk_mul_f32 v[216:217], v[116:117], v[216:217]
	v_pk_mul_f32 v[218:219], v[118:119], v[218:219]
	v_cvt_pk_bf16_f32 v192, v212, v213
	v_cvt_pk_bf16_f32 v193, v214, v215
	v_cvt_pk_bf16_f32 v194, v216, v217
	v_cvt_pk_bf16_f32 v195, v218, v219
	global_store_dwordx4 v253, v[192:195], s[12:13]
	s_waitcnt vmcnt(15)
	v_cvt_f32_ubyte0_e32 v212, v238
	v_cvt_f32_ubyte1_e32 v213, v238
	v_cvt_f32_ubyte2_e32 v214, v238
	v_cvt_f32_ubyte3_e32 v215, v238
	v_cvt_f32_ubyte0_e32 v216, v239
	v_cvt_f32_ubyte1_e32 v217, v239
	v_cvt_f32_ubyte2_e32 v218, v239
	v_cvt_f32_ubyte3_e32 v219, v239
	v_max_f32_e32 v212, 0x3985b185, v212
	v_max_f32_e32 v213, 0x3985b185, v213
	v_max_f32_e32 v214, 0x3985b185, v214
	v_max_f32_e32 v215, 0x3985b185, v215
	v_max_f32_e32 v216, 0x3985b185, v216
	v_max_f32_e32 v217, 0x3985b185, v217
	v_max_f32_e32 v218, 0x3985b185, v218
	v_max_f32_e32 v219, 0x3985b185, v219
	v_pk_mul_f32 v[212:213], v[212:213], s[54:55] op_sel_hi:[1,0]
	v_pk_mul_f32 v[214:215], v[214:215], s[54:55] op_sel_hi:[1,0]
	v_pk_mul_f32 v[216:217], v[216:217], s[54:55] op_sel_hi:[1,0]
	v_pk_mul_f32 v[218:219], v[218:219], s[54:55] op_sel_hi:[1,0]
	v_pk_mul_f32 v[212:213], v[144:145], v[212:213]
	v_pk_mul_f32 v[214:215], v[146:147], v[214:215]
	v_pk_mul_f32 v[216:217], v[140:141], v[216:217]
	v_pk_mul_f32 v[218:219], v[142:143], v[218:219]
	v_cvt_pk_bf16_f32 v196, v212, v213
	v_cvt_pk_bf16_f32 v197, v214, v215
	v_cvt_pk_bf16_f32 v198, v216, v217
	v_cvt_pk_bf16_f32 v199, v218, v219
	global_store_dwordx4 v253, v[196:199], s[12:13] offset:256
	v_add_u32_e32 v253, 0x8000, v253
	s_waitcnt vmcnt(15)
	v_cvt_f32_ubyte0_e32 v212, v240
	v_cvt_f32_ubyte1_e32 v213, v240
	v_cvt_f32_ubyte2_e32 v214, v240
	v_cvt_f32_ubyte3_e32 v215, v240
	v_cvt_f32_ubyte0_e32 v216, v241
	v_cvt_f32_ubyte1_e32 v217, v241
	v_cvt_f32_ubyte2_e32 v218, v241
	v_cvt_f32_ubyte3_e32 v219, v241
	v_max_f32_e32 v212, 0x3985b185, v212
	v_max_f32_e32 v213, 0x3985b185, v213
	v_max_f32_e32 v214, 0x3985b185, v214
	v_max_f32_e32 v215, 0x3985b185, v215
	v_max_f32_e32 v216, 0x3985b185, v216
	v_max_f32_e32 v217, 0x3985b185, v217
	v_max_f32_e32 v218, 0x3985b185, v218
	v_max_f32_e32 v219, 0x3985b185, v219
	v_pk_mul_f32 v[212:213], v[212:213], s[54:55] op_sel_hi:[1,0]
	v_pk_mul_f32 v[214:215], v[214:215], s[54:55] op_sel_hi:[1,0]
	v_pk_mul_f32 v[216:217], v[216:217], s[54:55] op_sel_hi:[1,0]
	v_pk_mul_f32 v[218:219], v[218:219], s[54:55] op_sel_hi:[1,0]
	v_pk_mul_f32 v[212:213], v[128:129], v[212:213]
	v_pk_mul_f32 v[214:215], v[130:131], v[214:215]
	v_pk_mul_f32 v[216:217], v[124:125], v[216:217]
	v_pk_mul_f32 v[218:219], v[126:127], v[218:219]
	v_cvt_pk_bf16_f32 v192, v212, v213
	v_cvt_pk_bf16_f32 v193, v214, v215
	v_cvt_pk_bf16_f32 v194, v216, v217
	v_cvt_pk_bf16_f32 v195, v218, v219
	global_store_dwordx4 v253, v[192:195], s[12:13]
	s_waitcnt vmcnt(15)
; __device__ __forceinline__ u32x4 pack8(const f32x4 a, const f32x4 b) { u32x4 w; w.x = cvt_pk_bf16(a[0], a[1]); w.y = cvt_pk_bf16(a[2], a[3]); w.z = cvt_pk_bf16(b[0], b[1]); w.w = cvt_pk_bf16(b[2], b[3]); return w; }
;     __device__ __forceinline__ void operator()(f32x4 (&acc)[2][2][4][2], const Unit& u, int wr, int wc, int fr, int fq) const {
;     ...
;                 for (int bj = 0; bj < 2; ++bj) { const u32x2 a2 = ga[c & 1][m2][bj], b2 = gb[c & 1][m2][bj]; const float q = 1.0f / 255.0f;
;                     const f32x4 sa0 = {(float)((a2.x >> 0) & 0xffu), (float)((a2.x >> 8) & 0xffu), (float)((a2.x >> 16) & 0xffu), (float)((a2.x >> 24) & 0xffu)};
;                     const f32x4 sa1 = {(float)((a2.y >> 0) & 0xffu), (float)((a2.y >> 8) & 0xffu), (float)((a2.y >> 16) & 0xffu), (float)((a2.y >> 24) & 0xffu)};
;                     f32x4 sb0 = {(float)((b2.x >> 0) & 0xffu), (float)((b2.x >> 8) & 0xffu), (float)((b2.x >> 16) & 0xffu), (float)((b2.x >> 24) & 0xffu)};
;                     f32x4 sb1 = {(float)((b2.y >> 0) & 0xffu), (float)((b2.y >> 8) & 0xffu), (float)((b2.y >> 16) & 0xffu), (float)((b2.y >> 24) & 0xffu)};
; #pragma unroll
;                     for (int e = 0; e < 4; ++e) { sb0[e] = fmaxf(sb0[e], 2.55e-4f); sb1[e] = fmaxf(sb1[e], 2.55e-4f); }
;                     if (second) *(u32x4*)(MERGED + (size_t)(row0 + ai * HALF + m * 16) * DM + col0 + bj * HALF) = pack8(acc[ai][bj][m][0] * (sb0 * q), acc[ai][bj][m][1] * (sb1 * q));
	v_cvt_f32_ubyte0_e32 v212, v242
	v_cvt_f32_ubyte1_e32 v213, v242
	v_cvt_f32_ubyte2_e32 v214, v242
	v_cvt_f32_ubyte3_e32 v215, v242
	v_cvt_f32_ubyte0_e32 v216, v243
	v_cvt_f32_ubyte1_e32 v217, v243
	v_cvt_f32_ubyte2_e32 v218, v243
	v_cvt_f32_ubyte3_e32 v219, v243
	v_max_f32_e32 v212, 0x3985b185, v212
	v_max_f32_e32 v213, 0x3985b185, v213
	v_max_f32_e32 v214, 0x3985b185, v214
	v_max_f32_e32 v215, 0x3985b185, v215
	v_max_f32_e32 v216, 0x3985b185, v216
	v_max_f32_e32 v217, 0x3985b185, v217
	v_max_f32_e32 v218, 0x3985b185, v218
	v_max_f32_e32 v219, 0x3985b185, v219
	v_pk_mul_f32 v[212:213], v[212:213], s[54:55] op_sel_hi:[1,0]
	v_pk_mul_f32 v[214:215], v[214:215], s[54:55] op_sel_hi:[1,0]
	v_pk_mul_f32 v[216:217], v[216:217], s[54:55] op_sel_hi:[1,0]
	v_pk_mul_f32 v[218:219], v[218:219], s[54:55] op_sel_hi:[1,0]
	v_pk_mul_f32 v[212:213], v[112:113], v[212:213]
	v_pk_mul_f32 v[214:215], v[114:115], v[214:215]
	v_pk_mul_f32 v[216:217], v[108:109], v[216:217]
	v_pk_mul_f32 v[218:219], v[110:111], v[218:219]
	v_cvt_pk_bf16_f32 v196, v212, v213
	v_cvt_pk_bf16_f32 v197, v214, v215
	v_cvt_pk_bf16_f32 v198, v216, v217
	v_cvt_pk_bf16_f32 v199, v218, v219
	global_store_dwordx4 v253, v[196:199], s[12:13] offset:256
	v_add_u32_e32 v253, 0x28000, v253
	s_waitcnt vmcnt(15)
	v_cvt_f32_ubyte0_e32 v212, v244
	v_cvt_f32_ubyte1_e32 v213, v244
	v_cvt_f32_ubyte2_e32 v214, v244
	v_cvt_f32_ubyte3_e32 v215, v244
	v_cvt_f32_ubyte0_e32 v216, v245
	v_cvt_f32_ubyte1_e32 v217, v245
	v_cvt_f32_ubyte2_e32 v218, v245
	v_cvt_f32_ubyte3_e32 v219, v245
	v_max_f32_e32 v212, 0x3985b185, v212
	v_max_f32_e32 v213, 0x3985b185, v213
	v_max_f32_e32 v214, 0x3985b185, v214
	v_max_f32_e32 v215, 0x3985b185, v215
	v_max_f32_e32 v216, 0x3985b185, v216
	v_max_f32_e32 v217, 0x3985b185, v217
	v_max_f32_e32 v218, 0x3985b185, v218
	v_max_f32_e32 v219, 0x3985b185, v219
	v_pk_mul_f32 v[212:213], v[212:213], s[54:55] op_sel_hi:[1,0]
	v_pk_mul_f32 v[214:215], v[214:215], s[54:55] op_sel_hi:[1,0]
	v_pk_mul_f32 v[216:217], v[216:217], s[54:55] op_sel_hi:[1,0]
	v_pk_mul_f32 v[218:219], v[218:219], s[54:55] op_sel_hi:[1,0]
	v_pk_mul_f32 v[212:213], v[96:97], v[212:213]
	v_pk_mul_f32 v[214:215], v[98:99], v[214:215]
	v_pk_mul_f32 v[216:217], v[92:93], v[216:217]
	v_pk_mul_f32 v[218:219], v[94:95], v[218:219]
	v_cvt_pk_bf16_f32 v192, v212, v213
	v_cvt_pk_bf16_f32 v193, v214, v215
	v_cvt_pk_bf16_f32 v194, v216, v217
	v_cvt_pk_bf16_f32 v195, v218, v219
	global_store_dwordx4 v253, v[192:195], s[12:13]
	s_waitcnt vmcnt(15)
	v_cvt_f32_ubyte0_e32 v212, v246
	v_cvt_f32_ubyte1_e32 v213, v246
	v_cvt_f32_ubyte2_e32 v214, v246
	v_cvt_f32_ubyte3_e32 v215, v246
	v_cvt_f32_ubyte0_e32 v216, v247
	v_cvt_f32_ubyte1_e32 v217, v247
	v_cvt_f32_ubyte2_e32 v218, v247
	v_cvt_f32_ubyte3_e32 v219, v247
	v_max_f32_e32 v212, 0x3985b185, v212
	v_max_f32_e32 v213, 0x3985b185, v213
	v_max_f32_e32 v214, 0x3985b185, v214
	v_max_f32_e32 v215, 0x3985b185, v215
	v_max_f32_e32 v216, 0x3985b185, v216
	v_max_f32_e32 v217, 0x3985b185, v217
	v_max_f32_e32 v218, 0x3985b185, v218
	v_max_f32_e32 v219, 0x3985b185, v219
	v_pk_mul_f32 v[212:213], v[212:213], s[54:55] op_sel_hi:[1,0]
	v_pk_mul_f32 v[214:215], v[214:215], s[54:55] op_sel_hi:[1,0]
	v_pk_mul_f32 v[216:217], v[216:217], s[54:55] op_sel_hi:[1,0]
	v_pk_mul_f32 v[218:219], v[218:219], s[54:55] op_sel_hi:[1,0]
	v_pk_mul_f32 v[212:213], v[80:81], v[212:213]
	v_pk_mul_f32 v[214:215], v[82:83], v[214:215]
	v_pk_mul_f32 v[216:217], v[76:77], v[216:217]
	v_pk_mul_f32 v[218:219], v[78:79], v[218:219]
	v_cvt_pk_bf16_f32 v196, v212, v213
	v_cvt_pk_bf16_f32 v197, v214, v215
	v_cvt_pk_bf16_f32 v198, v216, v217
	v_cvt_pk_bf16_f32 v199, v218, v219
	global_store_dwordx4 v253, v[196:199], s[12:13] offset:256
	v_add_u32_e32 v253, 0x8000, v253
	s_waitcnt vmcnt(15)
	v_cvt_f32_ubyte0_e32 v212, v248
	v_cvt_f32_ubyte1_e32 v213, v248
	v_cvt_f32_ubyte2_e32 v214, v248
	v_cvt_f32_ubyte3_e32 v215, v248
	v_cvt_f32_ubyte0_e32 v216, v249
	v_cvt_f32_ubyte1_e32 v217, v249
	v_cvt_f32_ubyte2_e32 v218, v249
	v_cvt_f32_ubyte3_e32 v219, v249
	v_max_f32_e32 v212, 0x3985b185, v212
	v_max_f32_e32 v213, 0x3985b185, v213
	v_max_f32_e32 v214, 0x3985b185, v214
	v_max_f32_e32 v215, 0x3985b185, v215
	v_max_f32_e32 v216, 0x3985b185, v216
	v_max_f32_e32 v217, 0x3985b185, v217
	v_max_f32_e32 v218, 0x3985b185, v218
	v_max_f32_e32 v219, 0x3985b185, v219
	v_pk_mul_f32 v[212:213], v[212:213], s[54:55] op_sel_hi:[1,0]
	v_pk_mul_f32 v[214:215], v[214:215], s[54:55] op_sel_hi:[1,0]
	v_pk_mul_f32 v[216:217], v[216:217], s[54:55] op_sel_hi:[1,0]
	v_pk_mul_f32 v[218:219], v[218:219], s[54:55] op_sel_hi:[1,0]
	v_pk_mul_f32 v[212:213], v[64:65], v[212:213]
	v_pk_mul_f32 v[214:215], v[66:67], v[214:215]
	v_pk_mul_f32 v[216:217], v[60:61], v[216:217]
	v_pk_mul_f32 v[218:219], v[62:63], v[218:219]
	v_cvt_pk_bf16_f32 v192, v212, v213
	v_cvt_pk_bf16_f32 v193, v214, v215
	v_cvt_pk_bf16_f32 v194, v216, v217
	v_cvt_pk_bf16_f32 v195, v218, v219
	global_store_dwordx4 v253, v[192:195], s[12:13]
	s_waitcnt vmcnt(15)
; __device__ __forceinline__ u32x4 pack8(const f32x4 a, const f32x4 b) { u32x4 w; w.x = cvt_pk_bf16(a[0], a[1]); w.y = cvt_pk_bf16(a[2], a[3]); w.z = cvt_pk_bf16(b[0], b[1]); w.w = cvt_pk_bf16(b[2], b[3]); return w; }
;     __device__ __forceinline__ void operator()(f32x4 (&acc)[2][2][4][2], const Unit& u, int wr, int wc, int fr, int fq) const {
;     ...
;                 for (int bj = 0; bj < 2; ++bj) { const u32x2 a2 = ga[c & 1][m2][bj], b2 = gb[c & 1][m2][bj]; const float q = 1.0f / 255.0f;
;                     const f32x4 sa0 = {(float)((a2.x >> 0) & 0xffu), (float)((a2.x >> 8) & 0xffu), (float)((a2.x >> 16) & 0xffu), (float)((a2.x >> 24) & 0xffu)};
;                     const f32x4 sa1 = {(float)((a2.y >> 0) & 0xffu), (float)((a2.y >> 8) & 0xffu), (float)((a2.y >> 16) & 0xffu), (float)((a2.y >> 24) & 0xffu)};
;                     f32x4 sb0 = {(float)((b2.x >> 0) & 0xffu), (float)((b2.x >> 8) & 0xffu), (float)((b2.x >> 16) & 0xffu), (float)((b2.x >> 24) & 0xffu)};
;                     f32x4 sb1 = {(float)((b2.y >> 0) & 0xffu), (float)((b2.y >> 8) & 0xffu), (float)((b2.y >> 16) & 0xffu), (float)((b2.y >> 24) & 0xffu)};
; #pragma unroll
;                     for (int e = 0; e < 4; ++e) { sb0[e] = fmaxf(sb0[e], 2.55e-4f); sb1[e] = fmaxf(sb1[e], 2.55e-4f); }
;                     if (second) *(u32x4*)(MERGED + (size_t)(row0 + ai * HALF + m * 16) * DM + col0 + bj * HALF) = pack8(acc[ai][bj][m][0] * (sb0 * q), acc[ai][bj][m][1] * (sb1 * q));
	v_cvt_f32_ubyte0_e32 v212, v250
	v_cvt_f32_ubyte1_e32 v213, v250
	v_cvt_f32_ubyte2_e32 v214, v250
	v_cvt_f32_ubyte3_e32 v215, v250
	v_cvt_f32_ubyte0_e32 v216, v251
	v_cvt_f32_ubyte1_e32 v217, v251
	v_cvt_f32_ubyte2_e32 v218, v251
	v_cvt_f32_ubyte3_e32 v219, v251
	v_max_f32_e32 v212, 0x3985b185, v212
	v_max_f32_e32 v213, 0x3985b185, v213
	v_max_f32_e32 v214, 0x3985b185, v214
	v_max_f32_e32 v215, 0x3985b185, v215
	v_max_f32_e32 v216, 0x3985b185, v216
	v_max_f32_e32 v217, 0x3985b185, v217
	v_max_f32_e32 v218, 0x3985b185, v218
	v_max_f32_e32 v219, 0x3985b185, v219
	v_pk_mul_f32 v[212:213], v[212:213], s[54:55] op_sel_hi:[1,0]
	v_pk_mul_f32 v[214:215], v[214:215], s[54:55] op_sel_hi:[1,0]
	v_pk_mul_f32 v[216:217], v[216:217], s[54:55] op_sel_hi:[1,0]
	v_pk_mul_f32 v[218:219], v[218:219], s[54:55] op_sel_hi:[1,0]
	v_pk_mul_f32 v[212:213], v[48:49], v[212:213]
	v_pk_mul_f32 v[214:215], v[50:51], v[214:215]
	v_pk_mul_f32 v[216:217], v[44:45], v[216:217]
	v_pk_mul_f32 v[218:219], v[46:47], v[218:219]
	v_cvt_pk_bf16_f32 v196, v212, v213
	v_cvt_pk_bf16_f32 v197, v214, v215
	v_cvt_pk_bf16_f32 v198, v216, v217
	v_cvt_pk_bf16_f32 v199, v218, v219
	global_store_dwordx4 v253, v[196:199], s[12:13] offset:256
	v_add_u32_e32 v253, 0x8000, v253
	s_waitcnt vmcnt(15)
	v_cvt_f32_ubyte0_e32 v212, v36
	v_cvt_f32_ubyte1_e32 v213, v36
	v_cvt_f32_ubyte2_e32 v214, v36
	v_cvt_f32_ubyte3_e32 v215, v36
	v_cvt_f32_ubyte0_e32 v216, v37
	v_cvt_f32_ubyte1_e32 v217, v37
	v_cvt_f32_ubyte2_e32 v218, v37
	v_cvt_f32_ubyte3_e32 v219, v37
	v_max_f32_e32 v212, 0x3985b185, v212
	v_max_f32_e32 v213, 0x3985b185, v213
	v_max_f32_e32 v214, 0x3985b185, v214
	v_max_f32_e32 v215, 0x3985b185, v215
	v_max_f32_e32 v216, 0x3985b185, v216
	v_max_f32_e32 v217, 0x3985b185, v217
	v_max_f32_e32 v218, 0x3985b185, v218
	v_max_f32_e32 v219, 0x3985b185, v219
	v_pk_mul_f32 v[212:213], v[212:213], s[54:55] op_sel_hi:[1,0]
	v_pk_mul_f32 v[214:215], v[214:215], s[54:55] op_sel_hi:[1,0]
	v_pk_mul_f32 v[216:217], v[216:217], s[54:55] op_sel_hi:[1,0]
	v_pk_mul_f32 v[218:219], v[218:219], s[54:55] op_sel_hi:[1,0]
	v_pk_mul_f32 v[212:213], v[32:33], v[212:213]
	v_pk_mul_f32 v[214:215], v[34:35], v[214:215]
	v_pk_mul_f32 v[216:217], v[28:29], v[216:217]
	v_pk_mul_f32 v[218:219], v[30:31], v[218:219]
	v_cvt_pk_bf16_f32 v192, v212, v213
	v_cvt_pk_bf16_f32 v193, v214, v215
	v_cvt_pk_bf16_f32 v194, v216, v217
	v_cvt_pk_bf16_f32 v195, v218, v219
	global_store_dwordx4 v253, v[192:195], s[12:13]
	s_waitcnt vmcnt(15)
	v_cvt_f32_ubyte0_e32 v212, v38
	v_cvt_f32_ubyte1_e32 v213, v38
	v_cvt_f32_ubyte2_e32 v214, v38
	v_cvt_f32_ubyte3_e32 v215, v38
	v_cvt_f32_ubyte0_e32 v216, v39
	v_cvt_f32_ubyte1_e32 v217, v39
	v_cvt_f32_ubyte2_e32 v218, v39
	v_cvt_f32_ubyte3_e32 v219, v39
	v_max_f32_e32 v212, 0x3985b185, v212
	v_max_f32_e32 v213, 0x3985b185, v213
	v_max_f32_e32 v214, 0x3985b185, v214
	v_max_f32_e32 v215, 0x3985b185, v215
	v_max_f32_e32 v216, 0x3985b185, v216
	v_max_f32_e32 v217, 0x3985b185, v217
	v_max_f32_e32 v218, 0x3985b185, v218
	v_max_f32_e32 v219, 0x3985b185, v219
	v_pk_mul_f32 v[212:213], v[212:213], s[54:55] op_sel_hi:[1,0]
	v_pk_mul_f32 v[214:215], v[214:215], s[54:55] op_sel_hi:[1,0]
	v_pk_mul_f32 v[216:217], v[216:217], s[54:55] op_sel_hi:[1,0]
	v_pk_mul_f32 v[218:219], v[218:219], s[54:55] op_sel_hi:[1,0]
	v_pk_mul_f32 v[212:213], v[24:25], v[212:213]
	v_pk_mul_f32 v[214:215], v[26:27], v[214:215]
	v_pk_mul_f32 v[216:217], v[20:21], v[216:217]
	v_pk_mul_f32 v[218:219], v[22:23], v[218:219]
	v_cvt_pk_bf16_f32 v196, v212, v213
	v_cvt_pk_bf16_f32 v197, v214, v215
	v_cvt_pk_bf16_f32 v198, v216, v217
	v_cvt_pk_bf16_f32 v199, v218, v219
	global_store_dwordx4 v253, v[196:199], s[12:13] offset:256
	v_add_u32_e32 v253, 0x8000, v253
	s_waitcnt vmcnt(15)
	v_cvt_f32_ubyte0_e32 v212, v40
	v_cvt_f32_ubyte1_e32 v213, v40
	v_cvt_f32_ubyte2_e32 v214, v40
	v_cvt_f32_ubyte3_e32 v215, v40
	v_cvt_f32_ubyte0_e32 v216, v41
	v_cvt_f32_ubyte1_e32 v217, v41
	v_cvt_f32_ubyte2_e32 v218, v41
	v_cvt_f32_ubyte3_e32 v219, v41
	v_max_f32_e32 v212, 0x3985b185, v212
	v_max_f32_e32 v213, 0x3985b185, v213
	v_max_f32_e32 v214, 0x3985b185, v214
	v_max_f32_e32 v215, 0x3985b185, v215
	v_max_f32_e32 v216, 0x3985b185, v216
	v_max_f32_e32 v217, 0x3985b185, v217
	v_max_f32_e32 v218, 0x3985b185, v218
	v_max_f32_e32 v219, 0x3985b185, v219
	v_pk_mul_f32 v[212:213], v[212:213], s[54:55] op_sel_hi:[1,0]
	v_pk_mul_f32 v[214:215], v[214:215], s[54:55] op_sel_hi:[1,0]
	v_pk_mul_f32 v[216:217], v[216:217], s[54:55] op_sel_hi:[1,0]
	v_pk_mul_f32 v[218:219], v[218:219], s[54:55] op_sel_hi:[1,0]
	v_pk_mul_f32 v[212:213], v[16:17], v[212:213]
	v_pk_mul_f32 v[214:215], v[18:19], v[214:215]
	v_pk_mul_f32 v[216:217], v[12:13], v[216:217]
	v_pk_mul_f32 v[218:219], v[14:15], v[218:219]
	v_cvt_pk_bf16_f32 v192, v212, v213
	v_cvt_pk_bf16_f32 v193, v214, v215
	v_cvt_pk_bf16_f32 v194, v216, v217
	v_cvt_pk_bf16_f32 v195, v218, v219
	global_store_dwordx4 v253, v[192:195], s[12:13]
	s_waitcnt vmcnt(15)
	v_cvt_f32_ubyte0_e32 v212, v42
	v_cvt_f32_ubyte1_e32 v213, v42
	v_cvt_f32_ubyte2_e32 v214, v42
	v_cvt_f32_ubyte3_e32 v215, v42
	v_cvt_f32_ubyte0_e32 v216, v43
	v_cvt_f32_ubyte1_e32 v217, v43
	v_cvt_f32_ubyte2_e32 v218, v43
	v_cvt_f32_ubyte3_e32 v219, v43
	v_max_f32_e32 v212, 0x3985b185, v212
	v_max_f32_e32 v213, 0x3985b185, v213
	v_max_f32_e32 v214, 0x3985b185, v214
	v_max_f32_e32 v215, 0x3985b185, v215
	v_max_f32_e32 v216, 0x3985b185, v216
	v_max_f32_e32 v217, 0x3985b185, v217
	v_max_f32_e32 v218, 0x3985b185, v218
	v_max_f32_e32 v219, 0x3985b185, v219
	v_pk_mul_f32 v[212:213], v[212:213], s[54:55] op_sel_hi:[1,0]
	v_pk_mul_f32 v[214:215], v[214:215], s[54:55] op_sel_hi:[1,0]
	v_pk_mul_f32 v[216:217], v[216:217], s[54:55] op_sel_hi:[1,0]
	v_pk_mul_f32 v[218:219], v[218:219], s[54:55] op_sel_hi:[1,0]
	v_pk_mul_f32 v[212:213], v[8:9], v[212:213]
	v_pk_mul_f32 v[214:215], v[10:11], v[214:215]
	v_pk_mul_f32 v[216:217], v[4:5], v[216:217]
	v_pk_mul_f32 v[218:219], v[6:7], v[218:219]
	v_cvt_pk_bf16_f32 v196, v212, v213
	v_cvt_pk_bf16_f32 v197, v214, v215
	v_cvt_pk_bf16_f32 v198, v216, v217
	v_cvt_pk_bf16_f32 v199, v218, v219
	global_store_dwordx4 v253, v[196:199], s[12:13] offset:256
